# speedup vs baseline: 1.0148x; 1.0105x over previous
.Lmy_loopb:
	ds_read_b128 v[158:161], v248 offset:0
	ds_read_b128 v[162:165], v248 offset:1024
	ds_read_b128 v[166:169], v249 offset:2048
	ds_read_b128 v[170:173], v249 offset:3072
	v_mfma_f32_16x16x32_f16 v[218:221], v[82:85], v[150:153], v[106:109]
	v_mfma_f32_16x16x32_f16 v[222:225], v[90:93], v[150:153], v[110:113]
	v_mfma_f32_16x16x32_f16 v[218:221], v[86:89], v[154:157], v[218:221]
	v_mfma_f32_16x16x32_f16 v[222:225], v[94:97], v[154:157], v[222:225]
	s_waitcnt lgkmcnt(2)
	v_mfma_f32_16x16x32_f16 v[210:213], v[54:57], v[158:161], v[210:213]
	v_mfma_f32_16x16x32_f16 v[210:213], v[58:61], v[162:165], v[210:213]
	s_waitcnt lgkmcnt(0)
	v_mfma_f32_16x16x32_f16 v[210:213], v[62:65], v[166:169], v[210:213]
	v_mfma_f32_16x16x32_f16 v[210:213], v[50:53], v[170:173], v[210:213]
	s_waitcnt vmcnt(9)
	v_cvt_pk_f16_f32 v251, v192, v193
	ds_write_b32 v1, v251 offset:0
	ds_read_b128 v[150:153], v186 offset:6144
	ds_read_b128 v[154:157], v186 offset:7168
	s_nop 2
	v_exp_f32_e32 v226, v210
	v_exp_f32_e32 v227, v211
	v_mfma_f32_16x16x32_f16 v[214:217], v[34:37], v[158:161], v[214:217]
	v_min_f32_e32 v228, s42, v212
	v_exp_f32_e32 v229, v213
	v_mfma_f32_16x16x32_f16 v[214:217], v[38:41], v[162:165], v[214:217]
	v_exp_f32_e32 v228, v228
	v_add_f32_e32 v227, 1.0, v227
	v_mfma_f32_16x16x32_f16 v[214:217], v[42:45], v[166:169], v[214:217]
	v_fma_f32 v230, v228, s41, s41
	v_rcp_f32_e32 v227, v227
	v_mfma_f32_16x16x32_f16 v[214:217], v[46:49], v[170:173], v[214:217]
	v_fma_f32 v230, v226, v230, v230
	v_rcp_f32_e32 v230, v230
	v_mfma_f32_16x16x32_f16 v[218:221], v[18:21], v[158:161], v[218:221]
	v_fma_f32 v226, -v228, v230, v230
	v_fma_f32 v200, v200, v227, v226
	v_mfma_f32_16x16x32_f16 v[218:221], v[14:17], v[162:165], v[218:221]
	v_exp_f32_e32 v226, v200
	s_nop 0
	v_add_f32_e32 v227, 1.0, v226
	v_mfma_f32_16x16x32_f16 v[218:221], v[10:13], v[166:169], v[218:221]
	v_fma_f32 v227, v229, v227, v227
	v_rcp_f32_e32 v227, v227
	v_mfma_f32_16x16x32_f16 v[218:221], v[26:29], v[170:173], v[218:221]
	v_fma_f32 v226, -v226, v227, v227
	v_exp_f32_e32 v231, v214
	v_mfma_f32_16x16x32_f16 v[222:225], v[2:5], v[158:161], v[222:225]
	v_exp_f32_e32 v232, v215
	v_min_f32_e32 v233, s42, v216
	v_mfma_f32_16x16x32_f16 v[222:225], v[6:9], v[162:165], v[222:225]
	v_exp_f32_e32 v234, v217
	v_exp_f32_e32 v233, v233
	v_mfma_f32_16x16x32_f16 v[222:225], v[22:25], v[166:169], v[222:225]
	v_exp_f32_e32 v236, v218
	v_add_f32_e32 v232, 1.0, v232
	v_mfma_f32_16x16x32_f16 v[222:225], v[30:33], v[170:173], v[222:225]
	v_fma_f32 v235, v233, s41, s41
	v_exp_f32_e32 v227, v219
	v_rcp_f32_e32 v232, v232
	v_fma_f32 v235, v231, v235, v235
	v_min_f32_e32 v228, s42, v220
	v_rcp_f32_e32 v235, v235
	s_nop 0
	v_fma_f32 v231, -v233, v235, v235
	v_exp_f32_e32 v229, v221
	v_fma_f32 v201, v201, v232, v231
	v_exp_f32_e32 v231, v201
	v_exp_f32_e32 v228, v228
	v_add_f32_e32 v232, 1.0, v231
	v_fma_f32 v232, v234, v232, v232
	v_add_f32_e32 v227, 1.0, v227
	v_rcp_f32_e32 v232, v232
	v_mfma_f32_16x16x32_f16 v[146:149], v[122:125], v[158:161], v[146:149]
	v_fma_f32 v231, -v231, v232, v232
	v_fma_f32 v230, v228, s41, s41
	v_cvt_pk_f16_f32 v246, v226, v231
	v_mfma_f32_16x16x32_f16 v[146:149], v[126:129], v[162:165], v[146:149]
	v_exp_f32_e32 v231, v222
	v_rcp_f32_e32 v227, v227
	v_exp_f32_e32 v232, v223
	buffer_load_dwordx4 v[122:125], v189, s[76:79], s46 offen
	buffer_load_dwordx4 v[126:129], v208, s[76:79], s46 offen
	v_min_f32_e32 v233, s42, v224
	v_fma_f32 v230, v236, v230, v230
	v_exp_f32_e32 v234, v225
	s_waitcnt lgkmcnt(0)
	v_mfma_f32_16x16x32_f16 v[210:213], v[70:73], v[150:153], v[98:101]
	v_exp_f32_e32 v233, v233
	v_rcp_f32_e32 v230, v230
	v_add_f32_e32 v232, 1.0, v232
	v_mfma_f32_16x16x32_f16 v[214:217], v[74:77], v[150:153], v[102:105]
	v_fma_f32 v235, v233, s41, s41
	v_fma_f32 v236, -v228, v230, v230
	v_rcp_f32_e32 v232, v232
	v_fma_f32 v235, v231, v235, v235
	v_fma_f32 v198, v198, v227, v236
	v_rcp_f32_e32 v235, v235
	s_nop 0
	v_fma_f32 v231, -v233, v235, v235
	v_exp_f32_e32 v236, v198
	v_fma_f32 v199, v199, v232, v231
	v_exp_f32_e32 v231, v199
	v_add_f32_e32 v227, 1.0, v236
	v_add_f32_e32 v232, 1.0, v231
	v_fma_f32 v232, v234, v232, v232
	v_fma_f32 v227, v229, v227, v227
	v_rcp_f32_e32 v232, v232
	s_nop 0
	v_fma_f32 v231, -v231, v232, v232
	v_rcp_f32_e32 v227, v227
	s_nop 0
	v_fma_f32 v236, -v236, v227, v227
	v_cvt_pk_f16_f32 v247, v236, v231
	ds_write_b64 v250, v[246:247] offset:12288
	v_mfma_f32_16x16x32_f16 v[210:213], v[66:69], v[154:157], v[210:213]
	v_mfma_f32_16x16x32_f16 v[214:217], v[78:81], v[154:157], v[214:217]
	buffer_load_dwordx2 v[192:193], v209, s[56:59], s45 offen
	s_waitcnt lgkmcnt(0)
	s_barrier
	ds_read_b128 v[158:161], v248 offset:4096
	ds_read_b128 v[162:165], v248 offset:5120
	ds_read_b128 v[166:169], v249 offset:6144
	ds_read_b128 v[170:173], v249 offset:7168
	v_mfma_f32_16x16x32_f16 v[218:221], v[82:85], v[150:153], v[106:109]
	v_mfma_f32_16x16x32_f16 v[222:225], v[90:93], v[150:153], v[110:113]
	v_mfma_f32_16x16x32_f16 v[218:221], v[86:89], v[154:157], v[218:221]
	v_mfma_f32_16x16x32_f16 v[222:225], v[94:97], v[154:157], v[222:225]
	s_waitcnt lgkmcnt(2)
	v_mfma_f32_16x16x32_f16 v[210:213], v[54:57], v[158:161], v[210:213]
	v_mfma_f32_16x16x32_f16 v[210:213], v[58:61], v[162:165], v[210:213]
	s_waitcnt lgkmcnt(0)
	v_mfma_f32_16x16x32_f16 v[210:213], v[62:65], v[166:169], v[210:213]
	v_mfma_f32_16x16x32_f16 v[210:213], v[50:53], v[170:173], v[210:213]
	s_waitcnt vmcnt(9)
	v_cvt_pk_f16_f32 v251, v190, v191
	ds_write_b32 v1, v251 offset:2048
	ds_read_b128 v[150:153], v186 offset:0
	ds_read_b128 v[154:157], v186 offset:1024
	s_nop 2
	v_exp_f32_e32 v226, v210
	v_exp_f32_e32 v227, v211
	v_mfma_f32_16x16x32_f16 v[214:217], v[34:37], v[158:161], v[214:217]
	v_min_f32_e32 v228, s42, v212
	v_exp_f32_e32 v229, v213
	v_mfma_f32_16x16x32_f16 v[214:217], v[38:41], v[162:165], v[214:217]
	v_exp_f32_e32 v228, v228
	v_add_f32_e32 v227, 1.0, v227
	v_mfma_f32_16x16x32_f16 v[214:217], v[42:45], v[166:169], v[214:217]
	v_fma_f32 v230, v228, s41, s41
	v_rcp_f32_e32 v227, v227
	v_mfma_f32_16x16x32_f16 v[214:217], v[46:49], v[170:173], v[214:217]
	v_fma_f32 v230, v226, v230, v230
	v_rcp_f32_e32 v230, v230
	v_mfma_f32_16x16x32_f16 v[218:221], v[18:21], v[158:161], v[218:221]
	v_fma_f32 v226, -v228, v230, v230
	v_fma_f32 v200, v200, v227, v226
	v_mfma_f32_16x16x32_f16 v[218:221], v[14:17], v[162:165], v[218:221]
	v_exp_f32_e32 v226, v200
	s_nop 0
	v_add_f32_e32 v227, 1.0, v226
	v_mfma_f32_16x16x32_f16 v[218:221], v[10:13], v[166:169], v[218:221]
	v_fma_f32 v227, v229, v227, v227
	v_rcp_f32_e32 v227, v227
	v_mfma_f32_16x16x32_f16 v[218:221], v[26:29], v[170:173], v[218:221]
	v_fma_f32 v226, -v226, v227, v227
	v_exp_f32_e32 v231, v214
	v_mfma_f32_16x16x32_f16 v[222:225], v[2:5], v[158:161], v[222:225]
	v_exp_f32_e32 v232, v215
	v_min_f32_e32 v233, s42, v216
	v_mfma_f32_16x16x32_f16 v[222:225], v[6:9], v[162:165], v[222:225]
	v_exp_f32_e32 v234, v217
	v_exp_f32_e32 v233, v233
	v_mfma_f32_16x16x32_f16 v[222:225], v[22:25], v[166:169], v[222:225]
	v_exp_f32_e32 v236, v218
	v_add_f32_e32 v232, 1.0, v232
	v_mfma_f32_16x16x32_f16 v[222:225], v[30:33], v[170:173], v[222:225]
	v_fma_f32 v235, v233, s41, s41
	v_exp_f32_e32 v227, v219
	v_rcp_f32_e32 v232, v232
	v_fma_f32 v235, v231, v235, v235
	v_min_f32_e32 v228, s42, v220
	v_rcp_f32_e32 v235, v235
	s_nop 0
	v_fma_f32 v231, -v233, v235, v235
	v_exp_f32_e32 v229, v221
	v_fma_f32 v201, v201, v232, v231
	v_exp_f32_e32 v231, v201
	v_exp_f32_e32 v228, v228
	v_add_f32_e32 v232, 1.0, v231
	v_fma_f32 v232, v234, v232, v232
	v_add_f32_e32 v227, 1.0, v227
	v_rcp_f32_e32 v232, v232
	v_mfma_f32_16x16x32_f16 v[146:149], v[114:117], v[158:161], v[146:149]
	v_fma_f32 v231, -v231, v232, v232
	v_fma_f32 v230, v228, s41, s41
	v_cvt_pk_f16_f32 v246, v226, v231
	v_mfma_f32_16x16x32_f16 v[146:149], v[118:121], v[162:165], v[146:149]
	v_exp_f32_e32 v231, v222
	v_rcp_f32_e32 v227, v227
	v_exp_f32_e32 v232, v223
	buffer_load_dwordx4 v[114:117], v189, s[80:83], s46 offen
	buffer_load_dwordx4 v[118:121], v208, s[80:83], s46 offen
	v_min_f32_e32 v233, s42, v224
	v_fma_f32 v230, v236, v230, v230
	v_exp_f32_e32 v234, v225
	s_waitcnt lgkmcnt(0)
	v_mfma_f32_16x16x32_f16 v[210:213], v[70:73], v[150:153], v[98:101]
	v_exp_f32_e32 v233, v233
	v_rcp_f32_e32 v230, v230
	v_add_f32_e32 v232, 1.0, v232
	v_mfma_f32_16x16x32_f16 v[214:217], v[74:77], v[150:153], v[102:105]
	v_fma_f32 v235, v233, s41, s41
	v_fma_f32 v236, -v228, v230, v230
	v_rcp_f32_e32 v232, v232
	v_fma_f32 v235, v231, v235, v235
	v_fma_f32 v198, v198, v227, v236
	v_rcp_f32_e32 v235, v235
	s_nop 0
	v_fma_f32 v231, -v233, v235, v235
	v_exp_f32_e32 v236, v198
	v_fma_f32 v199, v199, v232, v231
	v_exp_f32_e32 v231, v199
	v_add_f32_e32 v227, 1.0, v236
	v_add_f32_e32 v232, 1.0, v231
	v_fma_f32 v232, v234, v232, v232
	v_fma_f32 v227, v229, v227, v227
	v_rcp_f32_e32 v232, v232
	s_nop 0
	v_fma_f32 v231, -v231, v232, v232
	v_rcp_f32_e32 v227, v227
	s_nop 0
	v_fma_f32 v236, -v236, v227, v227
	v_cvt_pk_f16_f32 v247, v236, v231
	ds_write_b64 v250, v[246:247] offset:16384
	v_mfma_f32_16x16x32_f16 v[210:213], v[66:69], v[154:157], v[210:213]
	v_mfma_f32_16x16x32_f16 v[214:217], v[78:81], v[154:157], v[214:217]
	buffer_load_dwordx2 v[190:191], v209, s[60:63], s45 offen
	s_add_i32 s45, s45, 0x400000
	s_add_i32 s46, s46, 0x10000
	s_waitcnt lgkmcnt(0)
	s_barrier
	ds_read_b128 v[158:161], v248 offset:8192
	ds_read_b128 v[162:165], v248 offset:9216
	ds_read_b128 v[166:169], v249 offset:10240
	ds_read_b128 v[170:173], v249 offset:11264
	v_mfma_f32_16x16x32_f16 v[218:221], v[82:85], v[150:153], v[106:109]
	v_mfma_f32_16x16x32_f16 v[222:225], v[90:93], v[150:153], v[110:113]
	v_mfma_f32_16x16x32_f16 v[218:221], v[86:89], v[154:157], v[218:221]
	v_mfma_f32_16x16x32_f16 v[222:225], v[94:97], v[154:157], v[222:225]
	s_waitcnt lgkmcnt(2)
	v_mfma_f32_16x16x32_f16 v[210:213], v[54:57], v[158:161], v[210:213]
	v_mfma_f32_16x16x32_f16 v[210:213], v[58:61], v[162:165], v[210:213]
	s_waitcnt lgkmcnt(0)
	v_mfma_f32_16x16x32_f16 v[210:213], v[62:65], v[166:169], v[210:213]
	v_mfma_f32_16x16x32_f16 v[210:213], v[50:53], v[170:173], v[210:213]
	s_waitcnt vmcnt(9)
	v_cvt_pk_f16_f32 v251, v196, v197
	ds_write_b32 v1, v251 offset:4096
	ds_read_b128 v[150:153], v186 offset:2048
	ds_read_b128 v[154:157], v186 offset:3072
	s_nop 2
	v_exp_f32_e32 v226, v210
	v_exp_f32_e32 v227, v211
	v_mfma_f32_16x16x32_f16 v[214:217], v[34:37], v[158:161], v[214:217]
	v_min_f32_e32 v228, s42, v212
	v_exp_f32_e32 v229, v213
	v_mfma_f32_16x16x32_f16 v[214:217], v[38:41], v[162:165], v[214:217]
	v_exp_f32_e32 v228, v228
	v_add_f32_e32 v227, 1.0, v227
	v_mfma_f32_16x16x32_f16 v[214:217], v[42:45], v[166:169], v[214:217]
	v_fma_f32 v230, v228, s41, s41
	v_rcp_f32_e32 v227, v227
	v_mfma_f32_16x16x32_f16 v[214:217], v[46:49], v[170:173], v[214:217]
	v_fma_f32 v230, v226, v230, v230
	v_rcp_f32_e32 v230, v230
	v_mfma_f32_16x16x32_f16 v[218:221], v[18:21], v[158:161], v[218:221]
	v_fma_f32 v226, -v228, v230, v230
	v_fma_f32 v200, v200, v227, v226
	v_mfma_f32_16x16x32_f16 v[218:221], v[14:17], v[162:165], v[218:221]
	v_exp_f32_e32 v226, v200
	s_nop 0
	v_add_f32_e32 v227, 1.0, v226
	v_mfma_f32_16x16x32_f16 v[218:221], v[10:13], v[166:169], v[218:221]
	v_fma_f32 v227, v229, v227, v227
	v_rcp_f32_e32 v227, v227
	v_mfma_f32_16x16x32_f16 v[218:221], v[26:29], v[170:173], v[218:221]
	v_fma_f32 v226, -v226, v227, v227
	v_exp_f32_e32 v231, v214
	v_mfma_f32_16x16x32_f16 v[222:225], v[2:5], v[158:161], v[222:225]
	v_exp_f32_e32 v232, v215
	v_min_f32_e32 v233, s42, v216
	v_mfma_f32_16x16x32_f16 v[222:225], v[6:9], v[162:165], v[222:225]
	v_exp_f32_e32 v234, v217
	v_exp_f32_e32 v233, v233
	v_mfma_f32_16x16x32_f16 v[222:225], v[22:25], v[166:169], v[222:225]
	v_exp_f32_e32 v236, v218
	v_add_f32_e32 v232, 1.0, v232
	v_mfma_f32_16x16x32_f16 v[222:225], v[30:33], v[170:173], v[222:225]
	v_fma_f32 v235, v233, s41, s41
	v_exp_f32_e32 v227, v219
	v_rcp_f32_e32 v232, v232
	v_fma_f32 v235, v231, v235, v235
	v_min_f32_e32 v228, s42, v220
	v_rcp_f32_e32 v235, v235
	s_nop 0
	v_fma_f32 v231, -v233, v235, v235
	v_exp_f32_e32 v229, v221
	v_fma_f32 v201, v201, v232, v231
	v_exp_f32_e32 v231, v201
	v_exp_f32_e32 v228, v228
	v_add_f32_e32 v232, 1.0, v231
	v_fma_f32 v232, v234, v232, v232
	v_add_f32_e32 v227, 1.0, v227
	v_rcp_f32_e32 v232, v232
	v_mfma_f32_16x16x32_f16 v[146:149], v[138:141], v[158:161], v[146:149]
	v_fma_f32 v231, -v231, v232, v232
	v_fma_f32 v230, v228, s41, s41
	v_cvt_pk_f16_f32 v246, v226, v231
	v_mfma_f32_16x16x32_f16 v[146:149], v[142:145], v[162:165], v[146:149]
	v_exp_f32_e32 v231, v222
	v_rcp_f32_e32 v227, v227
	v_exp_f32_e32 v232, v223
	buffer_load_dwordx4 v[138:141], v189, s[68:71], s46 offen
	buffer_load_dwordx4 v[142:145], v208, s[68:71], s46 offen
	v_min_f32_e32 v233, s42, v224
	v_fma_f32 v230, v236, v230, v230
	v_exp_f32_e32 v234, v225
	s_waitcnt lgkmcnt(0)
	v_mfma_f32_16x16x32_f16 v[210:213], v[70:73], v[150:153], v[98:101]
	v_exp_f32_e32 v233, v233
	v_rcp_f32_e32 v230, v230
	v_add_f32_e32 v232, 1.0, v232
	v_mfma_f32_16x16x32_f16 v[214:217], v[74:77], v[150:153], v[102:105]
	v_fma_f32 v235, v233, s41, s41
	v_fma_f32 v236, -v228, v230, v230
	v_rcp_f32_e32 v232, v232
	v_fma_f32 v235, v231, v235, v235
	v_fma_f32 v198, v198, v227, v236
	v_rcp_f32_e32 v235, v235
	s_nop 0
	v_fma_f32 v231, -v233, v235, v235
	v_exp_f32_e32 v236, v198
	v_fma_f32 v199, v199, v232, v231
	v_exp_f32_e32 v231, v199
	v_add_f32_e32 v227, 1.0, v236
	v_add_f32_e32 v232, 1.0, v231
	v_fma_f32 v232, v234, v232, v232
	v_fma_f32 v227, v229, v227, v227
	v_rcp_f32_e32 v232, v232
	s_nop 0
	v_fma_f32 v231, -v231, v232, v232
	v_rcp_f32_e32 v227, v227
	s_nop 0
	v_fma_f32 v236, -v236, v227, v227
	v_cvt_pk_f16_f32 v247, v236, v231
	ds_write_b64 v250, v[246:247] offset:20480
	v_mfma_f32_16x16x32_f16 v[210:213], v[66:69], v[154:157], v[210:213]
	v_mfma_f32_16x16x32_f16 v[214:217], v[78:81], v[154:157], v[214:217]
	buffer_load_dwordx2 v[196:197], v209, s[48:51], s45 offen
	s_waitcnt lgkmcnt(0)
	s_barrier
	ds_read_b128 v[158:161], v248 offset:12288
	ds_read_b128 v[162:165], v248 offset:13312
	ds_read_b128 v[166:169], v249 offset:14336
	ds_read_b128 v[170:173], v249 offset:15360
	v_mfma_f32_16x16x32_f16 v[218:221], v[82:85], v[150:153], v[106:109]
	v_mfma_f32_16x16x32_f16 v[222:225], v[90:93], v[150:153], v[110:113]
	v_mfma_f32_16x16x32_f16 v[218:221], v[86:89], v[154:157], v[218:221]
	v_mfma_f32_16x16x32_f16 v[222:225], v[94:97], v[154:157], v[222:225]
	s_waitcnt lgkmcnt(2)
	v_mfma_f32_16x16x32_f16 v[210:213], v[54:57], v[158:161], v[210:213]
	v_mfma_f32_16x16x32_f16 v[210:213], v[58:61], v[162:165], v[210:213]
	s_waitcnt lgkmcnt(0)
	v_mfma_f32_16x16x32_f16 v[210:213], v[62:65], v[166:169], v[210:213]
	v_mfma_f32_16x16x32_f16 v[210:213], v[50:53], v[170:173], v[210:213]
	s_waitcnt vmcnt(9)
	v_cvt_pk_f16_f32 v251, v194, v195
	ds_write_b32 v1, v251 offset:6144
	ds_read_b128 v[150:153], v186 offset:4096
	ds_read_b128 v[154:157], v186 offset:5120
	s_nop 2
	v_exp_f32_e32 v226, v210
	v_exp_f32_e32 v227, v211
	v_mfma_f32_16x16x32_f16 v[214:217], v[34:37], v[158:161], v[214:217]
	v_min_f32_e32 v228, s42, v212
	v_exp_f32_e32 v229, v213
	v_mfma_f32_16x16x32_f16 v[214:217], v[38:41], v[162:165], v[214:217]
	v_exp_f32_e32 v228, v228
	v_add_f32_e32 v227, 1.0, v227
	v_mfma_f32_16x16x32_f16 v[214:217], v[42:45], v[166:169], v[214:217]
	v_fma_f32 v230, v228, s41, s41
	v_rcp_f32_e32 v227, v227
	v_mfma_f32_16x16x32_f16 v[214:217], v[46:49], v[170:173], v[214:217]
	v_fma_f32 v230, v226, v230, v230
	v_rcp_f32_e32 v230, v230
	v_mfma_f32_16x16x32_f16 v[218:221], v[18:21], v[158:161], v[218:221]
	v_fma_f32 v226, -v228, v230, v230
	v_fma_f32 v200, v200, v227, v226
	v_mfma_f32_16x16x32_f16 v[218:221], v[14:17], v[162:165], v[218:221]
	v_exp_f32_e32 v226, v200
	s_nop 0
	v_add_f32_e32 v227, 1.0, v226
	v_mfma_f32_16x16x32_f16 v[218:221], v[10:13], v[166:169], v[218:221]
	v_fma_f32 v227, v229, v227, v227
	v_rcp_f32_e32 v227, v227
	v_mfma_f32_16x16x32_f16 v[218:221], v[26:29], v[170:173], v[218:221]
	v_fma_f32 v226, -v226, v227, v227
	v_exp_f32_e32 v231, v214
	v_mfma_f32_16x16x32_f16 v[222:225], v[2:5], v[158:161], v[222:225]
	v_exp_f32_e32 v232, v215
	v_min_f32_e32 v233, s42, v216
	v_mfma_f32_16x16x32_f16 v[222:225], v[6:9], v[162:165], v[222:225]
	v_exp_f32_e32 v234, v217
	v_exp_f32_e32 v233, v233
	v_mfma_f32_16x16x32_f16 v[222:225], v[22:25], v[166:169], v[222:225]
	v_exp_f32_e32 v236, v218
	v_add_f32_e32 v232, 1.0, v232
	v_mfma_f32_16x16x32_f16 v[222:225], v[30:33], v[170:173], v[222:225]
	v_fma_f32 v235, v233, s41, s41
	v_exp_f32_e32 v227, v219
	v_rcp_f32_e32 v232, v232
	v_fma_f32 v235, v231, v235, v235
	v_min_f32_e32 v228, s42, v220
	v_rcp_f32_e32 v235, v235
	s_nop 0
	v_fma_f32 v231, -v233, v235, v235
	v_exp_f32_e32 v229, v221
	v_fma_f32 v201, v201, v232, v231
	v_exp_f32_e32 v231, v201
	v_exp_f32_e32 v228, v228
	v_add_f32_e32 v232, 1.0, v231
	v_fma_f32 v232, v234, v232, v232
	v_add_f32_e32 v227, 1.0, v227
	v_rcp_f32_e32 v232, v232
	v_mfma_f32_16x16x32_f16 v[146:149], v[130:133], v[158:161], v[146:149]
	v_fma_f32 v231, -v231, v232, v232
	v_fma_f32 v230, v228, s41, s41
	v_cvt_pk_f16_f32 v246, v226, v231
	v_mfma_f32_16x16x32_f16 v[146:149], v[134:137], v[162:165], v[146:149]
	v_exp_f32_e32 v231, v222
	v_rcp_f32_e32 v227, v227
	v_exp_f32_e32 v232, v223
	buffer_load_dwordx4 v[130:133], v189, s[72:75], s46 offen
	buffer_load_dwordx4 v[134:137], v208, s[72:75], s46 offen
	v_min_f32_e32 v233, s42, v224
	v_fma_f32 v230, v236, v230, v230
	v_exp_f32_e32 v234, v225
	s_waitcnt lgkmcnt(0)
	v_mfma_f32_16x16x32_f16 v[210:213], v[70:73], v[150:153], v[98:101]
	v_exp_f32_e32 v233, v233
	v_rcp_f32_e32 v230, v230
	v_add_f32_e32 v232, 1.0, v232
	v_mfma_f32_16x16x32_f16 v[214:217], v[74:77], v[150:153], v[102:105]
	v_fma_f32 v235, v233, s41, s41
	v_fma_f32 v236, -v228, v230, v230
	v_rcp_f32_e32 v232, v232
	v_fma_f32 v235, v231, v235, v235
	v_fma_f32 v198, v198, v227, v236
	v_rcp_f32_e32 v235, v235
	s_nop 0
	v_fma_f32 v231, -v233, v235, v235
	v_exp_f32_e32 v236, v198
	v_fma_f32 v199, v199, v232, v231
	v_exp_f32_e32 v231, v199
	v_add_f32_e32 v227, 1.0, v236
	v_add_f32_e32 v232, 1.0, v231
	v_fma_f32 v232, v234, v232, v232
	v_fma_f32 v227, v229, v227, v227
	v_rcp_f32_e32 v232, v232
	s_nop 0
	v_fma_f32 v231, -v231, v232, v232
	v_rcp_f32_e32 v227, v227
	s_nop 0
	v_fma_f32 v236, -v236, v227, v227
	v_cvt_pk_f16_f32 v247, v236, v231
	ds_write_b64 v250, v[246:247] offset:24576
	v_mfma_f32_16x16x32_f16 v[210:213], v[66:69], v[154:157], v[210:213]
	v_mfma_f32_16x16x32_f16 v[214:217], v[78:81], v[154:157], v[214:217]
	buffer_load_dwordx2 v[194:195], v209, s[52:55], s45 offen
	v_add_u32_e32 v250, 0x4000, v250
	v_add_u32_e32 v248, 0x4000, v248
	v_add_u32_e32 v249, 0x4000, v249
	s_waitcnt lgkmcnt(0)
	s_barrier
	s_cmp_lt_u32 s46, 0xa0000
	s_cbranch_scc1 .Lmy_loopb
	ds_read_b128 v[158:161], v248 offset:0
	ds_read_b128 v[162:165], v248 offset:1024
	ds_read_b128 v[166:169], v249 offset:2048
	ds_read_b128 v[170:173], v249 offset:3072
	v_mfma_f32_16x16x32_f16 v[218:221], v[82:85], v[150:153], v[106:109]
	v_mfma_f32_16x16x32_f16 v[222:225], v[90:93], v[150:153], v[110:113]
	v_mfma_f32_16x16x32_f16 v[218:221], v[86:89], v[154:157], v[218:221]
	v_mfma_f32_16x16x32_f16 v[222:225], v[94:97], v[154:157], v[222:225]
	s_waitcnt lgkmcnt(2)
	v_mfma_f32_16x16x32_f16 v[210:213], v[54:57], v[158:161], v[210:213]
	v_mfma_f32_16x16x32_f16 v[210:213], v[58:61], v[162:165], v[210:213]
	s_waitcnt lgkmcnt(0)
	v_mfma_f32_16x16x32_f16 v[210:213], v[62:65], v[166:169], v[210:213]
	v_mfma_f32_16x16x32_f16 v[210:213], v[50:53], v[170:173], v[210:213]
	s_waitcnt vmcnt(9)
	v_cvt_pk_f16_f32 v251, v192, v193
	ds_write_b32 v1, v251 offset:0
	ds_read_b128 v[150:153], v186 offset:6144
	ds_read_b128 v[154:157], v186 offset:7168
	s_nop 2
	v_exp_f32_e32 v226, v210
	v_exp_f32_e32 v227, v211
	v_mfma_f32_16x16x32_f16 v[214:217], v[34:37], v[158:161], v[214:217]
	v_min_f32_e32 v228, s42, v212
	v_exp_f32_e32 v229, v213
	v_mfma_f32_16x16x32_f16 v[214:217], v[38:41], v[162:165], v[214:217]
	v_exp_f32_e32 v228, v228
	v_add_f32_e32 v227, 1.0, v227
	v_mfma_f32_16x16x32_f16 v[214:217], v[42:45], v[166:169], v[214:217]
	v_fma_f32 v230, v228, s41, s41
	v_rcp_f32_e32 v227, v227
	v_mfma_f32_16x16x32_f16 v[214:217], v[46:49], v[170:173], v[214:217]
	v_fma_f32 v230, v226, v230, v230
	v_rcp_f32_e32 v230, v230
	v_mfma_f32_16x16x32_f16 v[218:221], v[18:21], v[158:161], v[218:221]
	v_fma_f32 v226, -v228, v230, v230
	v_fma_f32 v200, v200, v227, v226
	v_mfma_f32_16x16x32_f16 v[218:221], v[14:17], v[162:165], v[218:221]
	v_min_f32_e32 v226, s42, v200
	v_exp_f32_e32 v226, v226
	v_mfma_f32_16x16x32_f16 v[218:221], v[10:13], v[166:169], v[218:221]
	v_add_f32_e32 v227, 1.0, v226
	v_fma_f32 v227, v229, v227, v227
	v_mfma_f32_16x16x32_f16 v[218:221], v[26:29], v[170:173], v[218:221]
	v_rcp_f32_e32 v227, v227
	v_exp_f32_e32 v231, v214
	v_mfma_f32_16x16x32_f16 v[222:225], v[2:5], v[158:161], v[222:225]
	v_exp_f32_e32 v232, v215
	v_fma_f32 v226, -v226, v227, v227
	v_mfma_f32_16x16x32_f16 v[222:225], v[6:9], v[162:165], v[222:225]
	v_min_f32_e32 v233, s42, v216
	v_exp_f32_e32 v234, v217
	v_mfma_f32_16x16x32_f16 v[222:225], v[22:25], v[166:169], v[222:225]
	v_exp_f32_e32 v236, v218
	v_exp_f32_e32 v233, v233
	v_mfma_f32_16x16x32_f16 v[222:225], v[30:33], v[170:173], v[222:225]
	v_add_f32_e32 v232, 1.0, v232
	v_exp_f32_e32 v227, v219
	v_fma_f32 v235, v233, s41, s41
	v_rcp_f32_e32 v232, v232
	v_min_f32_e32 v228, s42, v220
	v_fma_f32 v235, v231, v235, v235
	v_rcp_f32_e32 v235, v235
	v_exp_f32_e32 v229, v221
	v_fma_f32 v231, -v233, v235, v235
	v_fma_f32 v201, v201, v232, v231
	v_exp_f32_e32 v228, v228
	v_min_f32_e32 v231, s42, v201
	v_exp_f32_e32 v231, v231
	v_add_f32_e32 v227, 1.0, v227
	v_add_f32_e32 v232, 1.0, v231
	v_mfma_f32_16x16x32_f16 v[146:149], v[122:125], v[158:161], v[146:149]
	v_fma_f32 v232, v234, v232, v232
	v_fma_f32 v230, v228, s41, s41
	v_rcp_f32_e32 v232, v232
	v_mfma_f32_16x16x32_f16 v[146:149], v[126:129], v[162:165], v[146:149]
	v_fma_f32 v231, -v231, v232, v232
	v_rcp_f32_e32 v227, v227
	v_cvt_pk_f16_f32 v246, v226, v231
	buffer_load_dwordx4 v[122:125], v189, s[76:79], s46 offen
	buffer_load_dwordx4 v[126:129], v208, s[76:79], s46 offen
	v_exp_f32_e32 v231, v222
	v_fma_f32 v230, v236, v230, v230
	v_exp_f32_e32 v232, v223
	s_waitcnt lgkmcnt(0)
	v_mfma_f32_16x16x32_f16 v[210:213], v[70:73], v[150:153], v[98:101]
	v_min_f32_e32 v233, s42, v224
	v_rcp_f32_e32 v230, v230
	v_exp_f32_e32 v234, v225
	v_mfma_f32_16x16x32_f16 v[214:217], v[74:77], v[150:153], v[102:105]
	v_exp_f32_e32 v233, v233
	v_fma_f32 v236, -v228, v230, v230
	v_add_f32_e32 v232, 1.0, v232
	v_fma_f32 v235, v233, s41, s41
	v_fma_f32 v198, v198, v227, v236
	v_rcp_f32_e32 v232, v232
	v_fma_f32 v235, v231, v235, v235
	v_min_f32_e32 v236, s42, v198
	v_rcp_f32_e32 v235, v235
	s_nop 0
	v_fma_f32 v231, -v233, v235, v235
	v_exp_f32_e32 v236, v236
	v_fma_f32 v199, v199, v232, v231
	v_min_f32_e32 v231, s42, v199
	v_add_f32_e32 v227, 1.0, v236
	v_exp_f32_e32 v231, v231
	v_fma_f32 v227, v229, v227, v227
	v_add_f32_e32 v232, 1.0, v231
	v_rcp_f32_e32 v227, v227
	v_fma_f32 v232, v234, v232, v232
	v_fma_f32 v236, -v236, v227, v227
	v_rcp_f32_e32 v232, v232
	s_nop 0
	v_fma_f32 v231, -v231, v232, v232
	v_cvt_pk_f16_f32 v247, v236, v231
	ds_write_b64 v250, v[246:247] offset:12288
	v_mfma_f32_16x16x32_f16 v[210:213], v[66:69], v[154:157], v[210:213]
	v_mfma_f32_16x16x32_f16 v[214:217], v[78:81], v[154:157], v[214:217]
	buffer_load_dwordx2 v[192:193], v209, s[56:59], s45 offen
	s_waitcnt lgkmcnt(0)
	s_barrier
	ds_read_b128 v[158:161], v248 offset:4096
	ds_read_b128 v[162:165], v248 offset:5120
	ds_read_b128 v[166:169], v249 offset:6144
	ds_read_b128 v[170:173], v249 offset:7168
	v_mfma_f32_16x16x32_f16 v[218:221], v[82:85], v[150:153], v[106:109]
	v_mfma_f32_16x16x32_f16 v[222:225], v[90:93], v[150:153], v[110:113]
	v_mfma_f32_16x16x32_f16 v[218:221], v[86:89], v[154:157], v[218:221]
	v_mfma_f32_16x16x32_f16 v[222:225], v[94:97], v[154:157], v[222:225]
	s_waitcnt lgkmcnt(2)
	v_mfma_f32_16x16x32_f16 v[210:213], v[54:57], v[158:161], v[210:213]
	v_mfma_f32_16x16x32_f16 v[210:213], v[58:61], v[162:165], v[210:213]
	s_waitcnt lgkmcnt(0)
	v_mfma_f32_16x16x32_f16 v[210:213], v[62:65], v[166:169], v[210:213]
	v_mfma_f32_16x16x32_f16 v[210:213], v[50:53], v[170:173], v[210:213]
	s_waitcnt vmcnt(9)
	v_cvt_pk_f16_f32 v251, v190, v191
	ds_write_b32 v1, v251 offset:2048
	ds_read_b128 v[150:153], v186 offset:0
	ds_read_b128 v[154:157], v186 offset:1024
	s_nop 2
	v_exp_f32_e32 v226, v210
	v_exp_f32_e32 v227, v211
	v_mfma_f32_16x16x32_f16 v[214:217], v[34:37], v[158:161], v[214:217]
	v_min_f32_e32 v228, s42, v212
	v_exp_f32_e32 v229, v213
	v_mfma_f32_16x16x32_f16 v[214:217], v[38:41], v[162:165], v[214:217]
	v_exp_f32_e32 v228, v228
	v_add_f32_e32 v227, 1.0, v227
	v_mfma_f32_16x16x32_f16 v[214:217], v[42:45], v[166:169], v[214:217]
	v_fma_f32 v230, v228, s41, s41
	v_rcp_f32_e32 v227, v227
	v_mfma_f32_16x16x32_f16 v[214:217], v[46:49], v[170:173], v[214:217]
	v_fma_f32 v230, v226, v230, v230
	v_rcp_f32_e32 v230, v230
	v_mfma_f32_16x16x32_f16 v[218:221], v[18:21], v[158:161], v[218:221]
	v_fma_f32 v226, -v228, v230, v230
	v_fma_f32 v200, v200, v227, v226
	v_mfma_f32_16x16x32_f16 v[218:221], v[14:17], v[162:165], v[218:221]
	v_min_f32_e32 v226, s42, v200
	v_exp_f32_e32 v226, v226
	v_mfma_f32_16x16x32_f16 v[218:221], v[10:13], v[166:169], v[218:221]
	v_add_f32_e32 v227, 1.0, v226
	v_fma_f32 v227, v229, v227, v227
	v_mfma_f32_16x16x32_f16 v[218:221], v[26:29], v[170:173], v[218:221]
	v_rcp_f32_e32 v227, v227
	v_exp_f32_e32 v231, v214
	v_mfma_f32_16x16x32_f16 v[222:225], v[2:5], v[158:161], v[222:225]
	v_exp_f32_e32 v232, v215
	v_fma_f32 v226, -v226, v227, v227
	v_mfma_f32_16x16x32_f16 v[222:225], v[6:9], v[162:165], v[222:225]
	v_min_f32_e32 v233, s42, v216
	v_exp_f32_e32 v234, v217
	v_mfma_f32_16x16x32_f16 v[222:225], v[22:25], v[166:169], v[222:225]
	v_exp_f32_e32 v236, v218
	v_exp_f32_e32 v233, v233
	v_mfma_f32_16x16x32_f16 v[222:225], v[30:33], v[170:173], v[222:225]
	v_add_f32_e32 v232, 1.0, v232
	v_exp_f32_e32 v227, v219
	v_fma_f32 v235, v233, s41, s41
	v_rcp_f32_e32 v232, v232
	v_min_f32_e32 v228, s42, v220
	v_fma_f32 v235, v231, v235, v235
	v_rcp_f32_e32 v235, v235
	v_exp_f32_e32 v229, v221
	v_fma_f32 v231, -v233, v235, v235
	v_fma_f32 v201, v201, v232, v231
	v_exp_f32_e32 v228, v228
	v_min_f32_e32 v231, s42, v201
	v_exp_f32_e32 v231, v231
	v_add_f32_e32 v227, 1.0, v227
	v_add_f32_e32 v232, 1.0, v231
	v_mfma_f32_16x16x32_f16 v[146:149], v[114:117], v[158:161], v[146:149]
	v_fma_f32 v232, v234, v232, v232
	v_fma_f32 v230, v228, s41, s41
	v_rcp_f32_e32 v232, v232
	v_mfma_f32_16x16x32_f16 v[146:149], v[118:121], v[162:165], v[146:149]
	v_fma_f32 v231, -v231, v232, v232
	v_rcp_f32_e32 v227, v227
	v_cvt_pk_f16_f32 v246, v226, v231
	buffer_load_dwordx4 v[114:117], v189, s[80:83], s46 offen
	buffer_load_dwordx4 v[118:121], v208, s[80:83], s46 offen
	v_exp_f32_e32 v231, v222
	v_fma_f32 v230, v236, v230, v230
	v_exp_f32_e32 v232, v223
	s_waitcnt lgkmcnt(0)
	v_mfma_f32_16x16x32_f16 v[210:213], v[70:73], v[150:153], v[98:101]
	v_min_f32_e32 v233, s42, v224
	v_rcp_f32_e32 v230, v230
	v_exp_f32_e32 v234, v225
	v_mfma_f32_16x16x32_f16 v[214:217], v[74:77], v[150:153], v[102:105]
	v_exp_f32_e32 v233, v233
	v_fma_f32 v236, -v228, v230, v230
	v_add_f32_e32 v232, 1.0, v232
	v_fma_f32 v235, v233, s41, s41
	v_fma_f32 v198, v198, v227, v236
	v_rcp_f32_e32 v232, v232
	v_fma_f32 v235, v231, v235, v235
	v_min_f32_e32 v236, s42, v198
	v_rcp_f32_e32 v235, v235
	s_nop 0
	v_fma_f32 v231, -v233, v235, v235
	v_exp_f32_e32 v236, v236
	v_fma_f32 v199, v199, v232, v231
	v_min_f32_e32 v231, s42, v199
	v_add_f32_e32 v227, 1.0, v236
	v_exp_f32_e32 v231, v231
	v_fma_f32 v227, v229, v227, v227
	v_add_f32_e32 v232, 1.0, v231
	v_rcp_f32_e32 v227, v227
	v_fma_f32 v232, v234, v232, v232
	v_fma_f32 v236, -v236, v227, v227
	v_rcp_f32_e32 v232, v232
	s_nop 0
	v_fma_f32 v231, -v231, v232, v232
	v_cvt_pk_f16_f32 v247, v236, v231
	ds_write_b64 v250, v[246:247] offset:16384
	v_mfma_f32_16x16x32_f16 v[210:213], v[66:69], v[154:157], v[210:213]
	v_mfma_f32_16x16x32_f16 v[214:217], v[78:81], v[154:157], v[214:217]
	buffer_load_dwordx2 v[190:191], v209, s[60:63], s45 offen
	s_add_i32 s45, s45, 0x400000
	s_add_i32 s46, s46, 0x10000
	s_waitcnt lgkmcnt(0)
	s_barrier
	ds_read_b128 v[158:161], v248 offset:8192
	ds_read_b128 v[162:165], v248 offset:9216
	ds_read_b128 v[166:169], v249 offset:10240
	ds_read_b128 v[170:173], v249 offset:11264
	v_mfma_f32_16x16x32_f16 v[218:221], v[82:85], v[150:153], v[106:109]
	v_mfma_f32_16x16x32_f16 v[222:225], v[90:93], v[150:153], v[110:113]
	v_mfma_f32_16x16x32_f16 v[218:221], v[86:89], v[154:157], v[218:221]
	v_mfma_f32_16x16x32_f16 v[222:225], v[94:97], v[154:157], v[222:225]
	s_waitcnt lgkmcnt(2)
	v_mfma_f32_16x16x32_f16 v[210:213], v[54:57], v[158:161], v[210:213]
	v_mfma_f32_16x16x32_f16 v[210:213], v[58:61], v[162:165], v[210:213]
	s_waitcnt lgkmcnt(0)
	v_mfma_f32_16x16x32_f16 v[210:213], v[62:65], v[166:169], v[210:213]
	v_mfma_f32_16x16x32_f16 v[210:213], v[50:53], v[170:173], v[210:213]
	s_waitcnt vmcnt(9)
	v_cvt_pk_f16_f32 v251, v196, v197
	ds_write_b32 v1, v251 offset:4096
	ds_read_b128 v[150:153], v186 offset:2048
	ds_read_b128 v[154:157], v186 offset:3072
	s_nop 2
	v_exp_f32_e32 v226, v210
	v_exp_f32_e32 v227, v211
	v_mfma_f32_16x16x32_f16 v[214:217], v[34:37], v[158:161], v[214:217]
	v_min_f32_e32 v228, s42, v212
	v_exp_f32_e32 v229, v213
	v_mfma_f32_16x16x32_f16 v[214:217], v[38:41], v[162:165], v[214:217]
	v_exp_f32_e32 v228, v228
	v_add_f32_e32 v227, 1.0, v227
	v_mfma_f32_16x16x32_f16 v[214:217], v[42:45], v[166:169], v[214:217]
	v_fma_f32 v230, v228, s41, s41
	v_rcp_f32_e32 v227, v227
	v_mfma_f32_16x16x32_f16 v[214:217], v[46:49], v[170:173], v[214:217]
	v_fma_f32 v230, v226, v230, v230
	v_rcp_f32_e32 v230, v230
	v_mfma_f32_16x16x32_f16 v[218:221], v[18:21], v[158:161], v[218:221]
	v_fma_f32 v226, -v228, v230, v230
	v_fma_f32 v200, v200, v227, v226
	v_mfma_f32_16x16x32_f16 v[218:221], v[14:17], v[162:165], v[218:221]
	v_min_f32_e32 v226, s42, v200
	v_exp_f32_e32 v226, v226
	v_mfma_f32_16x16x32_f16 v[218:221], v[10:13], v[166:169], v[218:221]
	v_add_f32_e32 v227, 1.0, v226
	v_fma_f32 v227, v229, v227, v227
	v_mfma_f32_16x16x32_f16 v[218:221], v[26:29], v[170:173], v[218:221]
	v_rcp_f32_e32 v227, v227
	v_exp_f32_e32 v231, v214
	v_mfma_f32_16x16x32_f16 v[222:225], v[2:5], v[158:161], v[222:225]
	v_exp_f32_e32 v232, v215
	v_fma_f32 v226, -v226, v227, v227
	v_mfma_f32_16x16x32_f16 v[222:225], v[6:9], v[162:165], v[222:225]
	v_min_f32_e32 v233, s42, v216
	v_exp_f32_e32 v234, v217
	v_mfma_f32_16x16x32_f16 v[222:225], v[22:25], v[166:169], v[222:225]
	v_exp_f32_e32 v236, v218
	v_exp_f32_e32 v233, v233
	v_mfma_f32_16x16x32_f16 v[222:225], v[30:33], v[170:173], v[222:225]
	v_add_f32_e32 v232, 1.0, v232
	v_exp_f32_e32 v227, v219
	v_fma_f32 v235, v233, s41, s41
	v_rcp_f32_e32 v232, v232
	v_min_f32_e32 v228, s42, v220
	v_fma_f32 v235, v231, v235, v235
	v_rcp_f32_e32 v235, v235
	v_exp_f32_e32 v229, v221
	v_fma_f32 v231, -v233, v235, v235
	v_fma_f32 v201, v201, v232, v231
	v_exp_f32_e32 v228, v228
	v_min_f32_e32 v231, s42, v201
	v_exp_f32_e32 v231, v231
	v_add_f32_e32 v227, 1.0, v227
	v_add_f32_e32 v232, 1.0, v231
	v_mfma_f32_16x16x32_f16 v[146:149], v[138:141], v[158:161], v[146:149]
	v_fma_f32 v232, v234, v232, v232
	v_fma_f32 v230, v228, s41, s41
	v_rcp_f32_e32 v232, v232
	v_mfma_f32_16x16x32_f16 v[146:149], v[142:145], v[162:165], v[146:149]
	v_fma_f32 v231, -v231, v232, v232
	v_rcp_f32_e32 v227, v227
	v_cvt_pk_f16_f32 v246, v226, v231
	buffer_load_dwordx4 v[138:141], v189, s[68:71], s46 offen
	buffer_load_dwordx4 v[142:145], v208, s[68:71], s46 offen
	v_exp_f32_e32 v231, v222
	v_fma_f32 v230, v236, v230, v230
	v_exp_f32_e32 v232, v223
	s_waitcnt lgkmcnt(0)
	v_mfma_f32_16x16x32_f16 v[210:213], v[70:73], v[150:153], v[98:101]
	v_min_f32_e32 v233, s42, v224
	v_rcp_f32_e32 v230, v230
	v_exp_f32_e32 v234, v225
	v_mfma_f32_16x16x32_f16 v[214:217], v[74:77], v[150:153], v[102:105]
	v_exp_f32_e32 v233, v233
	v_fma_f32 v236, -v228, v230, v230
	v_add_f32_e32 v232, 1.0, v232
	v_fma_f32 v235, v233, s41, s41
	v_fma_f32 v198, v198, v227, v236
	v_rcp_f32_e32 v232, v232
	v_fma_f32 v235, v231, v235, v235
	v_min_f32_e32 v236, s42, v198
	v_rcp_f32_e32 v235, v235
	s_nop 0
	v_fma_f32 v231, -v233, v235, v235
	v_exp_f32_e32 v236, v236
	v_fma_f32 v199, v199, v232, v231
	v_min_f32_e32 v231, s42, v199
	v_add_f32_e32 v227, 1.0, v236
	v_exp_f32_e32 v231, v231
	v_fma_f32 v227, v229, v227, v227
	v_add_f32_e32 v232, 1.0, v231
	v_rcp_f32_e32 v227, v227
	v_fma_f32 v232, v234, v232, v232
	v_fma_f32 v236, -v236, v227, v227
	v_rcp_f32_e32 v232, v232
	s_nop 0
	v_fma_f32 v231, -v231, v232, v232
	v_cvt_pk_f16_f32 v247, v236, v231
	ds_write_b64 v250, v[246:247] offset:20480
	v_mfma_f32_16x16x32_f16 v[210:213], v[66:69], v[154:157], v[210:213]
	v_mfma_f32_16x16x32_f16 v[214:217], v[78:81], v[154:157], v[214:217]
	buffer_load_dwordx2 v[196:197], v209, s[48:51], s45 offen
	s_waitcnt lgkmcnt(0)
	s_barrier
	ds_read_b128 v[158:161], v248 offset:12288
	ds_read_b128 v[162:165], v248 offset:13312
	ds_read_b128 v[166:169], v249 offset:14336
	ds_read_b128 v[170:173], v249 offset:15360
	v_mfma_f32_16x16x32_f16 v[218:221], v[82:85], v[150:153], v[106:109]
	v_mfma_f32_16x16x32_f16 v[222:225], v[90:93], v[150:153], v[110:113]
	v_mfma_f32_16x16x32_f16 v[218:221], v[86:89], v[154:157], v[218:221]
	v_mfma_f32_16x16x32_f16 v[222:225], v[94:97], v[154:157], v[222:225]
	s_waitcnt lgkmcnt(2)
	v_mfma_f32_16x16x32_f16 v[210:213], v[54:57], v[158:161], v[210:213]
	v_mfma_f32_16x16x32_f16 v[210:213], v[58:61], v[162:165], v[210:213]
	s_waitcnt lgkmcnt(0)
	v_mfma_f32_16x16x32_f16 v[210:213], v[62:65], v[166:169], v[210:213]
	v_mfma_f32_16x16x32_f16 v[210:213], v[50:53], v[170:173], v[210:213]
	s_waitcnt vmcnt(9)
	v_cvt_pk_f16_f32 v251, v194, v195
	ds_write_b32 v1, v251 offset:6144
	ds_read_b128 v[150:153], v186 offset:4096
	ds_read_b128 v[154:157], v186 offset:5120
	s_nop 2
	v_exp_f32_e32 v226, v210
	v_exp_f32_e32 v227, v211
	v_mfma_f32_16x16x32_f16 v[214:217], v[34:37], v[158:161], v[214:217]
	v_min_f32_e32 v228, s42, v212
	v_exp_f32_e32 v229, v213
	v_mfma_f32_16x16x32_f16 v[214:217], v[38:41], v[162:165], v[214:217]
	v_exp_f32_e32 v228, v228
	v_add_f32_e32 v227, 1.0, v227
	v_mfma_f32_16x16x32_f16 v[214:217], v[42:45], v[166:169], v[214:217]
	v_fma_f32 v230, v228, s41, s41
	v_rcp_f32_e32 v227, v227
	v_mfma_f32_16x16x32_f16 v[214:217], v[46:49], v[170:173], v[214:217]
	v_fma_f32 v230, v226, v230, v230
	v_rcp_f32_e32 v230, v230
	v_mfma_f32_16x16x32_f16 v[218:221], v[18:21], v[158:161], v[218:221]
	v_fma_f32 v226, -v228, v230, v230
	v_fma_f32 v200, v200, v227, v226
	v_mfma_f32_16x16x32_f16 v[218:221], v[14:17], v[162:165], v[218:221]
	v_min_f32_e32 v226, s42, v200
	v_exp_f32_e32 v226, v226
	v_mfma_f32_16x16x32_f16 v[218:221], v[10:13], v[166:169], v[218:221]
	v_add_f32_e32 v227, 1.0, v226
	v_fma_f32 v227, v229, v227, v227
	v_mfma_f32_16x16x32_f16 v[218:221], v[26:29], v[170:173], v[218:221]
	v_rcp_f32_e32 v227, v227
	v_exp_f32_e32 v231, v214
	v_mfma_f32_16x16x32_f16 v[222:225], v[2:5], v[158:161], v[222:225]
	v_exp_f32_e32 v232, v215
	v_fma_f32 v226, -v226, v227, v227
	v_mfma_f32_16x16x32_f16 v[222:225], v[6:9], v[162:165], v[222:225]
	v_min_f32_e32 v233, s42, v216
	v_exp_f32_e32 v234, v217
	v_mfma_f32_16x16x32_f16 v[222:225], v[22:25], v[166:169], v[222:225]
	v_exp_f32_e32 v236, v218
	v_exp_f32_e32 v233, v233
	v_mfma_f32_16x16x32_f16 v[222:225], v[30:33], v[170:173], v[222:225]
	v_add_f32_e32 v232, 1.0, v232
	v_exp_f32_e32 v227, v219
	v_fma_f32 v235, v233, s41, s41
	v_rcp_f32_e32 v232, v232
	v_min_f32_e32 v228, s42, v220
	v_fma_f32 v235, v231, v235, v235
	v_rcp_f32_e32 v235, v235
	v_exp_f32_e32 v229, v221
	v_fma_f32 v231, -v233, v235, v235
	v_fma_f32 v201, v201, v232, v231
	v_exp_f32_e32 v228, v228
	v_min_f32_e32 v231, s42, v201
	v_exp_f32_e32 v231, v231
	v_add_f32_e32 v227, 1.0, v227
	v_add_f32_e32 v232, 1.0, v231
	v_mfma_f32_16x16x32_f16 v[146:149], v[130:133], v[158:161], v[146:149]
	v_fma_f32 v232, v234, v232, v232
	v_fma_f32 v230, v228, s41, s41
	v_rcp_f32_e32 v232, v232
	v_mfma_f32_16x16x32_f16 v[146:149], v[134:137], v[162:165], v[146:149]
	v_fma_f32 v231, -v231, v232, v232
	v_rcp_f32_e32 v227, v227
	v_cvt_pk_f16_f32 v246, v226, v231
	buffer_load_dwordx4 v[130:133], v189, s[72:75], s46 offen
	buffer_load_dwordx4 v[134:137], v208, s[72:75], s46 offen
	v_exp_f32_e32 v231, v222
	v_fma_f32 v230, v236, v230, v230
	v_exp_f32_e32 v232, v223
	s_waitcnt lgkmcnt(0)
	v_mfma_f32_16x16x32_f16 v[210:213], v[70:73], v[150:153], v[98:101]
	v_min_f32_e32 v233, s42, v224
	v_rcp_f32_e32 v230, v230
	v_exp_f32_e32 v234, v225
	v_mfma_f32_16x16x32_f16 v[214:217], v[74:77], v[150:153], v[102:105]
	v_exp_f32_e32 v233, v233
	v_fma_f32 v236, -v228, v230, v230
	v_add_f32_e32 v232, 1.0, v232
	v_fma_f32 v235, v233, s41, s41
	v_fma_f32 v198, v198, v227, v236
	v_rcp_f32_e32 v232, v232
	v_fma_f32 v235, v231, v235, v235
	v_min_f32_e32 v236, s42, v198
	v_rcp_f32_e32 v235, v235
	s_nop 0
	v_fma_f32 v231, -v233, v235, v235
	v_exp_f32_e32 v236, v236
	v_fma_f32 v199, v199, v232, v231
	v_min_f32_e32 v231, s42, v199
	v_add_f32_e32 v227, 1.0, v236
	v_exp_f32_e32 v231, v231
	v_fma_f32 v227, v229, v227, v227
	v_add_f32_e32 v232, 1.0, v231
	v_rcp_f32_e32 v227, v227
	v_fma_f32 v232, v234, v232, v232
	v_fma_f32 v236, -v236, v227, v227
	v_rcp_f32_e32 v232, v232
	s_nop 0
	v_fma_f32 v231, -v231, v232, v232
	v_cvt_pk_f16_f32 v247, v236, v231
	ds_write_b64 v250, v[246:247] offset:24576
	v_mfma_f32_16x16x32_f16 v[210:213], v[66:69], v[154:157], v[210:213]
	v_mfma_f32_16x16x32_f16 v[214:217], v[78:81], v[154:157], v[214:217]
	buffer_load_dwordx2 v[194:195], v209, s[52:55], s45 offen
	v_add_u32_e32 v250, 0x4000, v250
	v_add_u32_e32 v248, 0x4000, v248
	v_add_u32_e32 v249, 0x4000, v249
	s_waitcnt lgkmcnt(0)
	s_barrier
	ds_read_b128 v[158:161], v248 offset:0
	ds_read_b128 v[162:165], v248 offset:1024
	ds_read_b128 v[166:169], v249 offset:2048
	ds_read_b128 v[170:173], v249 offset:3072
	v_mfma_f32_16x16x32_f16 v[218:221], v[82:85], v[150:153], v[106:109]
	v_mfma_f32_16x16x32_f16 v[222:225], v[90:93], v[150:153], v[110:113]
	v_mfma_f32_16x16x32_f16 v[218:221], v[86:89], v[154:157], v[218:221]
	v_mfma_f32_16x16x32_f16 v[222:225], v[94:97], v[154:157], v[222:225]
	s_waitcnt lgkmcnt(2)
	v_mfma_f32_16x16x32_f16 v[210:213], v[54:57], v[158:161], v[210:213]
	v_mfma_f32_16x16x32_f16 v[210:213], v[58:61], v[162:165], v[210:213]
	s_waitcnt lgkmcnt(0)
	v_mfma_f32_16x16x32_f16 v[210:213], v[62:65], v[166:169], v[210:213]
	v_mfma_f32_16x16x32_f16 v[210:213], v[50:53], v[170:173], v[210:213]
	s_waitcnt vmcnt(9)
	v_cvt_pk_f16_f32 v251, v192, v193
	ds_write_b32 v1, v251 offset:0
	ds_read_b128 v[150:153], v186 offset:6144
	ds_read_b128 v[154:157], v186 offset:7168
	s_nop 2
	v_exp_f32_e32 v226, v210
	v_exp_f32_e32 v227, v211
	v_mfma_f32_16x16x32_f16 v[214:217], v[34:37], v[158:161], v[214:217]
	v_min_f32_e32 v228, s42, v212
	v_exp_f32_e32 v229, v213
	v_mfma_f32_16x16x32_f16 v[214:217], v[38:41], v[162:165], v[214:217]
	v_exp_f32_e32 v228, v228
	v_add_f32_e32 v227, 1.0, v227
	v_mfma_f32_16x16x32_f16 v[214:217], v[42:45], v[166:169], v[214:217]
	v_fma_f32 v230, v228, s41, s41
	v_rcp_f32_e32 v227, v227
	v_mfma_f32_16x16x32_f16 v[214:217], v[46:49], v[170:173], v[214:217]
	v_fma_f32 v230, v226, v230, v230
	v_rcp_f32_e32 v230, v230
	v_mfma_f32_16x16x32_f16 v[218:221], v[18:21], v[158:161], v[218:221]
	v_fma_f32 v226, -v228, v230, v230
	v_fma_f32 v200, v200, v227, v226
	v_mfma_f32_16x16x32_f16 v[218:221], v[14:17], v[162:165], v[218:221]
	v_min_f32_e32 v226, s42, v200
	v_exp_f32_e32 v226, v226
	v_mfma_f32_16x16x32_f16 v[218:221], v[10:13], v[166:169], v[218:221]
	v_add_f32_e32 v227, 1.0, v226
	v_fma_f32 v227, v229, v227, v227
	v_mfma_f32_16x16x32_f16 v[218:221], v[26:29], v[170:173], v[218:221]
	v_rcp_f32_e32 v227, v227
	v_exp_f32_e32 v231, v214
	v_mfma_f32_16x16x32_f16 v[222:225], v[2:5], v[158:161], v[222:225]
	v_exp_f32_e32 v232, v215
	v_fma_f32 v226, -v226, v227, v227
	v_mfma_f32_16x16x32_f16 v[222:225], v[6:9], v[162:165], v[222:225]
	v_min_f32_e32 v233, s42, v216
	v_exp_f32_e32 v234, v217
	v_mfma_f32_16x16x32_f16 v[222:225], v[22:25], v[166:169], v[222:225]
	v_exp_f32_e32 v236, v218
	v_exp_f32_e32 v233, v233
	v_mfma_f32_16x16x32_f16 v[222:225], v[30:33], v[170:173], v[222:225]
	v_add_f32_e32 v232, 1.0, v232
	v_exp_f32_e32 v227, v219
	v_fma_f32 v235, v233, s41, s41
	v_rcp_f32_e32 v232, v232
	v_min_f32_e32 v228, s42, v220
	v_fma_f32 v235, v231, v235, v235
	v_rcp_f32_e32 v235, v235
	v_exp_f32_e32 v229, v221
	v_fma_f32 v231, -v233, v235, v235
	v_fma_f32 v201, v201, v232, v231
	v_exp_f32_e32 v228, v228
	v_min_f32_e32 v231, s42, v201
	v_exp_f32_e32 v231, v231
	v_add_f32_e32 v227, 1.0, v227
	v_add_f32_e32 v232, 1.0, v231
	v_mfma_f32_16x16x32_f16 v[146:149], v[122:125], v[158:161], v[146:149]
	v_fma_f32 v232, v234, v232, v232
	v_fma_f32 v230, v228, s41, s41
	v_rcp_f32_e32 v232, v232
	v_mfma_f32_16x16x32_f16 v[146:149], v[126:129], v[162:165], v[146:149]
	v_fma_f32 v231, -v231, v232, v232
	v_rcp_f32_e32 v227, v227
	v_cvt_pk_f16_f32 v246, v226, v231
	buffer_load_dwordx4 v[122:125], v189, s[76:79], s46 offen
	buffer_load_dwordx4 v[126:129], v208, s[76:79], s46 offen
	v_exp_f32_e32 v231, v222
	v_fma_f32 v230, v236, v230, v230
	v_exp_f32_e32 v232, v223
	s_waitcnt lgkmcnt(0)
	v_mfma_f32_16x16x32_f16 v[210:213], v[70:73], v[150:153], v[98:101]
	v_min_f32_e32 v233, s42, v224
	v_rcp_f32_e32 v230, v230
	v_exp_f32_e32 v234, v225
	v_mfma_f32_16x16x32_f16 v[214:217], v[74:77], v[150:153], v[102:105]
	v_exp_f32_e32 v233, v233
	v_fma_f32 v236, -v228, v230, v230
	v_add_f32_e32 v232, 1.0, v232
	v_fma_f32 v235, v233, s41, s41
	v_fma_f32 v198, v198, v227, v236
	v_rcp_f32_e32 v232, v232
	v_fma_f32 v235, v231, v235, v235
	v_min_f32_e32 v236, s42, v198
	v_rcp_f32_e32 v235, v235
	s_nop 0
	v_fma_f32 v231, -v233, v235, v235
	v_exp_f32_e32 v236, v236
	v_fma_f32 v199, v199, v232, v231
	v_min_f32_e32 v231, s42, v199
	v_add_f32_e32 v227, 1.0, v236
	v_exp_f32_e32 v231, v231
	v_fma_f32 v227, v229, v227, v227
	v_add_f32_e32 v232, 1.0, v231
	v_rcp_f32_e32 v227, v227
	v_fma_f32 v232, v234, v232, v232
	v_fma_f32 v236, -v236, v227, v227
	v_rcp_f32_e32 v232, v232
	s_nop 0
	v_fma_f32 v231, -v231, v232, v232
	v_cvt_pk_f16_f32 v247, v236, v231
	ds_write_b64 v250, v[246:247] offset:12288
	v_mfma_f32_16x16x32_f16 v[210:213], v[66:69], v[154:157], v[210:213]
	v_mfma_f32_16x16x32_f16 v[214:217], v[78:81], v[154:157], v[214:217]
	buffer_load_dwordx2 v[192:193], v209, s[56:59], s45 offen
	s_waitcnt lgkmcnt(0)
	s_barrier
	ds_read_b128 v[158:161], v248 offset:4096
	ds_read_b128 v[162:165], v248 offset:5120
	ds_read_b128 v[166:169], v249 offset:6144
	ds_read_b128 v[170:173], v249 offset:7168
	v_mfma_f32_16x16x32_f16 v[218:221], v[82:85], v[150:153], v[106:109]
	v_mfma_f32_16x16x32_f16 v[222:225], v[90:93], v[150:153], v[110:113]
	v_mfma_f32_16x16x32_f16 v[218:221], v[86:89], v[154:157], v[218:221]
	v_mfma_f32_16x16x32_f16 v[222:225], v[94:97], v[154:157], v[222:225]
	s_waitcnt lgkmcnt(2)
	v_mfma_f32_16x16x32_f16 v[210:213], v[54:57], v[158:161], v[210:213]
	v_mfma_f32_16x16x32_f16 v[210:213], v[58:61], v[162:165], v[210:213]
	s_waitcnt lgkmcnt(0)
	v_mfma_f32_16x16x32_f16 v[210:213], v[62:65], v[166:169], v[210:213]
	v_mfma_f32_16x16x32_f16 v[210:213], v[50:53], v[170:173], v[210:213]
	s_waitcnt vmcnt(9)
	v_cvt_pk_f16_f32 v251, v190, v191
	ds_write_b32 v1, v251 offset:2048
	ds_read_b128 v[150:153], v186 offset:0
	ds_read_b128 v[154:157], v186 offset:1024
	s_nop 2
	v_exp_f32_e32 v226, v210
	v_exp_f32_e32 v227, v211
	v_mfma_f32_16x16x32_f16 v[214:217], v[34:37], v[158:161], v[214:217]
	v_min_f32_e32 v228, s42, v212
	v_exp_f32_e32 v229, v213
	v_mfma_f32_16x16x32_f16 v[214:217], v[38:41], v[162:165], v[214:217]
	v_exp_f32_e32 v228, v228
	v_add_f32_e32 v227, 1.0, v227
	v_mfma_f32_16x16x32_f16 v[214:217], v[42:45], v[166:169], v[214:217]
	v_fma_f32 v230, v228, s41, s41
	v_rcp_f32_e32 v227, v227
	v_mfma_f32_16x16x32_f16 v[214:217], v[46:49], v[170:173], v[214:217]
	v_fma_f32 v230, v226, v230, v230
	v_rcp_f32_e32 v230, v230
	v_mfma_f32_16x16x32_f16 v[218:221], v[18:21], v[158:161], v[218:221]
	v_fma_f32 v226, -v228, v230, v230
	v_fma_f32 v200, v200, v227, v226
	v_mfma_f32_16x16x32_f16 v[218:221], v[14:17], v[162:165], v[218:221]
	v_min_f32_e32 v226, s42, v200
	v_exp_f32_e32 v226, v226
	v_mfma_f32_16x16x32_f16 v[218:221], v[10:13], v[166:169], v[218:221]
	v_add_f32_e32 v227, 1.0, v226
	v_fma_f32 v227, v229, v227, v227
	v_mfma_f32_16x16x32_f16 v[218:221], v[26:29], v[170:173], v[218:221]
	v_rcp_f32_e32 v227, v227
	v_exp_f32_e32 v231, v214
	v_mfma_f32_16x16x32_f16 v[222:225], v[2:5], v[158:161], v[222:225]
	v_exp_f32_e32 v232, v215
	v_fma_f32 v226, -v226, v227, v227
	v_mfma_f32_16x16x32_f16 v[222:225], v[6:9], v[162:165], v[222:225]
	v_min_f32_e32 v233, s42, v216
	v_exp_f32_e32 v234, v217
	v_mfma_f32_16x16x32_f16 v[222:225], v[22:25], v[166:169], v[222:225]
	v_exp_f32_e32 v236, v218
	v_exp_f32_e32 v233, v233
	v_mfma_f32_16x16x32_f16 v[222:225], v[30:33], v[170:173], v[222:225]
	v_add_f32_e32 v232, 1.0, v232
	v_exp_f32_e32 v227, v219
	v_fma_f32 v235, v233, s41, s41
	v_rcp_f32_e32 v232, v232
	v_min_f32_e32 v228, s42, v220
	v_fma_f32 v235, v231, v235, v235
	v_rcp_f32_e32 v235, v235
	v_exp_f32_e32 v229, v221
	v_fma_f32 v231, -v233, v235, v235
	v_fma_f32 v201, v201, v232, v231
	v_exp_f32_e32 v228, v228
	v_min_f32_e32 v231, s42, v201
	v_exp_f32_e32 v231, v231
	v_add_f32_e32 v227, 1.0, v227
	v_add_f32_e32 v232, 1.0, v231
	v_mfma_f32_16x16x32_f16 v[146:149], v[114:117], v[158:161], v[146:149]
	v_fma_f32 v232, v234, v232, v232
	v_fma_f32 v230, v228, s41, s41
	v_rcp_f32_e32 v232, v232
	v_mfma_f32_16x16x32_f16 v[146:149], v[118:121], v[162:165], v[146:149]
	v_fma_f32 v231, -v231, v232, v232
	v_rcp_f32_e32 v227, v227
	v_cvt_pk_f16_f32 v246, v226, v231
	buffer_load_dwordx4 v[114:117], v189, s[80:83], s46 offen
	buffer_load_dwordx4 v[118:121], v208, s[80:83], s46 offen
	v_exp_f32_e32 v231, v222
	v_fma_f32 v230, v236, v230, v230
	v_exp_f32_e32 v232, v223
	s_waitcnt lgkmcnt(0)
	v_mfma_f32_16x16x32_f16 v[210:213], v[70:73], v[150:153], v[98:101]
	v_min_f32_e32 v233, s42, v224
	v_rcp_f32_e32 v230, v230
	v_exp_f32_e32 v234, v225
	v_mfma_f32_16x16x32_f16 v[214:217], v[74:77], v[150:153], v[102:105]
	v_exp_f32_e32 v233, v233
	v_fma_f32 v236, -v228, v230, v230
	v_add_f32_e32 v232, 1.0, v232
	v_fma_f32 v235, v233, s41, s41
	v_fma_f32 v198, v198, v227, v236
	v_rcp_f32_e32 v232, v232
	v_fma_f32 v235, v231, v235, v235
	v_min_f32_e32 v236, s42, v198
	v_rcp_f32_e32 v235, v235
	s_nop 0
	v_fma_f32 v231, -v233, v235, v235
	v_exp_f32_e32 v236, v236
	v_fma_f32 v199, v199, v232, v231
	v_min_f32_e32 v231, s42, v199
	v_add_f32_e32 v227, 1.0, v236
	v_exp_f32_e32 v231, v231
	v_fma_f32 v227, v229, v227, v227
	v_add_f32_e32 v232, 1.0, v231
	v_rcp_f32_e32 v227, v227
	v_fma_f32 v232, v234, v232, v232
	v_fma_f32 v236, -v236, v227, v227
	v_rcp_f32_e32 v232, v232
	s_nop 0
	v_fma_f32 v231, -v231, v232, v232
	v_cvt_pk_f16_f32 v247, v236, v231
	ds_write_b64 v250, v[246:247] offset:16384
	v_mfma_f32_16x16x32_f16 v[210:213], v[66:69], v[154:157], v[210:213]
	v_mfma_f32_16x16x32_f16 v[214:217], v[78:81], v[154:157], v[214:217]
	buffer_load_dwordx2 v[190:191], v209, s[60:63], s45 offen
	s_add_i32 s45, s45, 0x400000
	s_add_i32 s46, s46, 0x10000
	s_waitcnt lgkmcnt(0)
	s_barrier
	ds_read_b128 v[158:161], v248 offset:8192
	ds_read_b128 v[162:165], v248 offset:9216
	ds_read_b128 v[166:169], v249 offset:10240
	ds_read_b128 v[170:173], v249 offset:11264
	v_mfma_f32_16x16x32_f16 v[218:221], v[82:85], v[150:153], v[106:109]
	v_mfma_f32_16x16x32_f16 v[222:225], v[90:93], v[150:153], v[110:113]
	v_mfma_f32_16x16x32_f16 v[218:221], v[86:89], v[154:157], v[218:221]
	v_mfma_f32_16x16x32_f16 v[222:225], v[94:97], v[154:157], v[222:225]
	s_waitcnt lgkmcnt(2)
	v_mfma_f32_16x16x32_f16 v[210:213], v[54:57], v[158:161], v[210:213]
	v_mfma_f32_16x16x32_f16 v[210:213], v[58:61], v[162:165], v[210:213]
	s_waitcnt lgkmcnt(0)
	v_mfma_f32_16x16x32_f16 v[210:213], v[62:65], v[166:169], v[210:213]
	v_mfma_f32_16x16x32_f16 v[210:213], v[50:53], v[170:173], v[210:213]
	s_waitcnt vmcnt(9)
	v_cvt_pk_f16_f32 v251, v196, v197
	ds_write_b32 v1, v251 offset:4096
	ds_read_b128 v[150:153], v186 offset:2048
	ds_read_b128 v[154:157], v186 offset:3072
	s_nop 2
	v_exp_f32_e32 v226, v210
	v_exp_f32_e32 v227, v211
	v_mfma_f32_16x16x32_f16 v[214:217], v[34:37], v[158:161], v[214:217]
	v_min_f32_e32 v228, s42, v212
	v_exp_f32_e32 v229, v213
	v_mfma_f32_16x16x32_f16 v[214:217], v[38:41], v[162:165], v[214:217]
	v_exp_f32_e32 v228, v228
	v_add_f32_e32 v227, 1.0, v227
	v_mfma_f32_16x16x32_f16 v[214:217], v[42:45], v[166:169], v[214:217]
	v_fma_f32 v230, v228, s41, s41
	v_rcp_f32_e32 v227, v227
	v_mfma_f32_16x16x32_f16 v[214:217], v[46:49], v[170:173], v[214:217]
	v_fma_f32 v230, v226, v230, v230
	v_rcp_f32_e32 v230, v230
	v_mfma_f32_16x16x32_f16 v[218:221], v[18:21], v[158:161], v[218:221]
	v_fma_f32 v226, -v228, v230, v230
	v_fma_f32 v200, v200, v227, v226
	v_mfma_f32_16x16x32_f16 v[218:221], v[14:17], v[162:165], v[218:221]
	v_min_f32_e32 v226, s42, v200
	v_exp_f32_e32 v226, v226
	v_mfma_f32_16x16x32_f16 v[218:221], v[10:13], v[166:169], v[218:221]
	v_add_f32_e32 v227, 1.0, v226
	v_fma_f32 v227, v229, v227, v227
	v_mfma_f32_16x16x32_f16 v[218:221], v[26:29], v[170:173], v[218:221]
	v_rcp_f32_e32 v227, v227
	v_exp_f32_e32 v231, v214
	v_mfma_f32_16x16x32_f16 v[222:225], v[2:5], v[158:161], v[222:225]
	v_exp_f32_e32 v232, v215
	v_fma_f32 v226, -v226, v227, v227
	v_mfma_f32_16x16x32_f16 v[222:225], v[6:9], v[162:165], v[222:225]
	v_min_f32_e32 v233, s42, v216
	v_exp_f32_e32 v234, v217
	v_mfma_f32_16x16x32_f16 v[222:225], v[22:25], v[166:169], v[222:225]
	v_exp_f32_e32 v236, v218
	v_exp_f32_e32 v233, v233
	v_mfma_f32_16x16x32_f16 v[222:225], v[30:33], v[170:173], v[222:225]
	v_add_f32_e32 v232, 1.0, v232
	v_exp_f32_e32 v227, v219
	v_fma_f32 v235, v233, s41, s41
	v_rcp_f32_e32 v232, v232
	v_min_f32_e32 v228, s42, v220
	v_fma_f32 v235, v231, v235, v235
	v_rcp_f32_e32 v235, v235
	v_exp_f32_e32 v229, v221
	v_fma_f32 v231, -v233, v235, v235
	v_fma_f32 v201, v201, v232, v231
	v_exp_f32_e32 v228, v228
	v_min_f32_e32 v231, s42, v201
	v_exp_f32_e32 v231, v231
	v_add_f32_e32 v227, 1.0, v227
	v_add_f32_e32 v232, 1.0, v231
	v_mfma_f32_16x16x32_f16 v[146:149], v[138:141], v[158:161], v[146:149]
	v_fma_f32 v232, v234, v232, v232
	v_fma_f32 v230, v228, s41, s41
	v_rcp_f32_e32 v232, v232
	v_mfma_f32_16x16x32_f16 v[146:149], v[142:145], v[162:165], v[146:149]
	v_fma_f32 v231, -v231, v232, v232
	v_rcp_f32_e32 v227, v227
	v_cvt_pk_f16_f32 v246, v226, v231
	buffer_load_dwordx4 v[138:141], v189, s[68:71], s46 offen
	buffer_load_dwordx4 v[142:145], v208, s[68:71], s46 offen
	v_exp_f32_e32 v231, v222
	v_fma_f32 v230, v236, v230, v230
	v_exp_f32_e32 v232, v223
	s_waitcnt lgkmcnt(0)
	v_mfma_f32_16x16x32_f16 v[210:213], v[70:73], v[150:153], v[98:101]
	v_min_f32_e32 v233, s42, v224
	v_rcp_f32_e32 v230, v230
	v_exp_f32_e32 v234, v225
	v_mfma_f32_16x16x32_f16 v[214:217], v[74:77], v[150:153], v[102:105]
	v_exp_f32_e32 v233, v233
	v_fma_f32 v236, -v228, v230, v230
	v_add_f32_e32 v232, 1.0, v232
	v_fma_f32 v235, v233, s41, s41
	v_fma_f32 v198, v198, v227, v236
	v_rcp_f32_e32 v232, v232
	v_fma_f32 v235, v231, v235, v235
	v_min_f32_e32 v236, s42, v198
	v_rcp_f32_e32 v235, v235
	s_nop 0
	v_fma_f32 v231, -v233, v235, v235
	v_exp_f32_e32 v236, v236
	v_fma_f32 v199, v199, v232, v231
	v_min_f32_e32 v231, s42, v199
	v_add_f32_e32 v227, 1.0, v236
	v_exp_f32_e32 v231, v231
	v_fma_f32 v227, v229, v227, v227
	v_add_f32_e32 v232, 1.0, v231
	v_rcp_f32_e32 v227, v227
	v_fma_f32 v232, v234, v232, v232
	v_fma_f32 v236, -v236, v227, v227
	v_rcp_f32_e32 v232, v232
	s_nop 0
	v_fma_f32 v231, -v231, v232, v232
	v_cvt_pk_f16_f32 v247, v236, v231
	ds_write_b64 v250, v[246:247] offset:20480
	v_mfma_f32_16x16x32_f16 v[210:213], v[66:69], v[154:157], v[210:213]
	v_mfma_f32_16x16x32_f16 v[214:217], v[78:81], v[154:157], v[214:217]
	buffer_load_dwordx2 v[196:197], v209, s[48:51], s45 offen
	s_waitcnt lgkmcnt(0)
	s_barrier
	ds_read_b128 v[158:161], v248 offset:12288
	ds_read_b128 v[162:165], v248 offset:13312
	ds_read_b128 v[166:169], v249 offset:14336
	ds_read_b128 v[170:173], v249 offset:15360
	v_mfma_f32_16x16x32_f16 v[218:221], v[82:85], v[150:153], v[106:109]
	v_mfma_f32_16x16x32_f16 v[222:225], v[90:93], v[150:153], v[110:113]
	v_mfma_f32_16x16x32_f16 v[218:221], v[86:89], v[154:157], v[218:221]
	v_mfma_f32_16x16x32_f16 v[222:225], v[94:97], v[154:157], v[222:225]
	s_waitcnt lgkmcnt(2)
	v_mfma_f32_16x16x32_f16 v[210:213], v[54:57], v[158:161], v[210:213]
	v_mfma_f32_16x16x32_f16 v[210:213], v[58:61], v[162:165], v[210:213]
	s_waitcnt lgkmcnt(0)
	v_mfma_f32_16x16x32_f16 v[210:213], v[62:65], v[166:169], v[210:213]
	v_mfma_f32_16x16x32_f16 v[210:213], v[50:53], v[170:173], v[210:213]
	s_waitcnt vmcnt(9)
	s_nop 6
	v_exp_f32_e32 v226, v210
	v_exp_f32_e32 v227, v211
	v_mfma_f32_16x16x32_f16 v[214:217], v[34:37], v[158:161], v[214:217]
	v_min_f32_e32 v228, s42, v212
	v_exp_f32_e32 v229, v213
	v_mfma_f32_16x16x32_f16 v[214:217], v[38:41], v[162:165], v[214:217]
	v_exp_f32_e32 v228, v228
	v_add_f32_e32 v227, 1.0, v227
	v_mfma_f32_16x16x32_f16 v[214:217], v[42:45], v[166:169], v[214:217]
	v_fma_f32 v230, v228, s41, s41
	v_rcp_f32_e32 v227, v227
	v_mfma_f32_16x16x32_f16 v[214:217], v[46:49], v[170:173], v[214:217]
	v_fma_f32 v230, v226, v230, v230
	v_rcp_f32_e32 v230, v230
	v_mfma_f32_16x16x32_f16 v[218:221], v[18:21], v[158:161], v[218:221]
	v_fma_f32 v226, -v228, v230, v230
	v_fma_f32 v200, v200, v227, v226
	v_mfma_f32_16x16x32_f16 v[218:221], v[14:17], v[162:165], v[218:221]
	v_min_f32_e32 v226, s42, v200
	v_exp_f32_e32 v226, v226
	v_mfma_f32_16x16x32_f16 v[218:221], v[10:13], v[166:169], v[218:221]
	v_add_f32_e32 v227, 1.0, v226
	v_fma_f32 v227, v229, v227, v227
	v_mfma_f32_16x16x32_f16 v[218:221], v[26:29], v[170:173], v[218:221]
	v_rcp_f32_e32 v227, v227
	v_exp_f32_e32 v231, v214
	v_mfma_f32_16x16x32_f16 v[222:225], v[2:5], v[158:161], v[222:225]
	v_exp_f32_e32 v232, v215
	v_fma_f32 v226, -v226, v227, v227
	v_mfma_f32_16x16x32_f16 v[222:225], v[6:9], v[162:165], v[222:225]
	v_min_f32_e32 v233, s42, v216
	v_exp_f32_e32 v234, v217
	v_mfma_f32_16x16x32_f16 v[222:225], v[22:25], v[166:169], v[222:225]
	v_exp_f32_e32 v236, v218
	v_exp_f32_e32 v233, v233
	v_mfma_f32_16x16x32_f16 v[222:225], v[30:33], v[170:173], v[222:225]
	v_add_f32_e32 v232, 1.0, v232
	v_exp_f32_e32 v227, v219
	v_fma_f32 v235, v233, s41, s41
	v_rcp_f32_e32 v232, v232
	v_min_f32_e32 v228, s42, v220
	v_fma_f32 v235, v231, v235, v235
	v_rcp_f32_e32 v235, v235
	v_exp_f32_e32 v229, v221
	v_fma_f32 v231, -v233, v235, v235
	v_fma_f32 v201, v201, v232, v231
	v_exp_f32_e32 v228, v228
	v_min_f32_e32 v231, s42, v201
	v_exp_f32_e32 v231, v231
	v_add_f32_e32 v227, 1.0, v227
	v_add_f32_e32 v232, 1.0, v231
	v_mfma_f32_16x16x32_f16 v[146:149], v[130:133], v[158:161], v[146:149]
	v_fma_f32 v232, v234, v232, v232
	v_fma_f32 v230, v228, s41, s41
	v_rcp_f32_e32 v232, v232
	v_mfma_f32_16x16x32_f16 v[146:149], v[134:137], v[162:165], v[146:149]
	v_fma_f32 v231, -v231, v232, v232
	v_rcp_f32_e32 v227, v227
	v_cvt_pk_f16_f32 v246, v226, v231
	v_exp_f32_e32 v231, v222
	v_fma_f32 v230, v236, v230, v230
	v_exp_f32_e32 v232, v223
	s_waitcnt lgkmcnt(0)
	v_min_f32_e32 v233, s42, v224
	v_rcp_f32_e32 v230, v230
	v_exp_f32_e32 v234, v225
	v_exp_f32_e32 v233, v233
	v_fma_f32 v236, -v228, v230, v230
	v_add_f32_e32 v232, 1.0, v232
	v_fma_f32 v235, v233, s41, s41
	v_fma_f32 v198, v198, v227, v236
	v_rcp_f32_e32 v232, v232
	v_fma_f32 v235, v231, v235, v235
	v_min_f32_e32 v236, s42, v198
	v_rcp_f32_e32 v235, v235
	s_nop 0
	v_fma_f32 v231, -v233, v235, v235
	v_exp_f32_e32 v236, v236
	v_fma_f32 v199, v199, v232, v231
	v_min_f32_e32 v231, s42, v199
	v_add_f32_e32 v227, 1.0, v236
	v_exp_f32_e32 v231, v231
	v_fma_f32 v227, v229, v227, v227
	v_add_f32_e32 v232, 1.0, v231
	v_rcp_f32_e32 v227, v227
	v_fma_f32 v232, v234, v232, v232
	v_fma_f32 v236, -v236, v227, v227
	v_rcp_f32_e32 v232, v232
	s_nop 0
	v_fma_f32 v231, -v231, v232, v232
	v_cvt_pk_f16_f32 v247, v236, v231
	ds_write_b64 v250, v[246:247] offset:24576
	v_add_u32_e32 v250, 0x4000, v250
	v_add_u32_e32 v248, 0x4000, v248
	v_add_u32_e32 v249, 0x4000, v249
	s_waitcnt lgkmcnt(0)
	s_barrier
	s_nop 7
	ds_read_b128 v[158:161], v248 offset:0
	ds_read_b128 v[162:165], v248 offset:1024
	s_lshr_b32 s48, s35, 5
	v_and_b32_e32 v211, 15, v0
	v_bfe_u32 v212, v0, 4, 2
	v_and_b32_e32 v213, 31, v0
	v_bfe_u32 v214, v0, 5, 1
	v_add_u32_e32 v214, s48, v214
	s_lshl_b32 s49, s35, 4
	s_addk_i32 s49, 0x2000
	v_lshl_add_u32 v215, v212, 8, s49
	v_lshl_add_u32 v215, v211, 2, v215
	v_lshlrev_b32_e32 v216, 6, v213
	v_lshl_add_u32 v216, v214, 2, v216
	v_mul_u32_u24_e32 v217, 0x110, v214
	v_lshl_add_u32 v217, v213, 2, v217
	v_mul_u32_u24_e32 v218, 0x110, v211
	v_add_u32_e32 v219, 0x4000, v206
	v_add_u32_e32 v220, 0x14000, v206
	v_add_u32_e32 v221, 0x24000, v206
	v_add_u32_e32 v222, s34, v211
	v_lshlrev_b32_e32 v222, 9, v222
	v_add_u32_e32 v222, s35, v222
	v_lshl_add_u32 v222, v212, 4, v222
	s_waitcnt vmcnt(7) lgkmcnt(0)
	v_mfma_f32_16x16x32_f16 v[146:149], v[122:125], v[158:161], v[146:149]
	v_mfma_f32_16x16x32_f16 v[146:149], v[126:129], v[162:165], v[146:149]
	ds_read_b64 v[30:31], v219 offset:0
	ds_read_b64 v[32:33], v219 offset:4096
	ds_read_b64 v[34:35], v219 offset:8192
	ds_read_b64 v[36:37], v219 offset:12288
	ds_read_b64 v[38:39], v219 offset:16384
	ds_read_b64 v[40:41], v219 offset:20480
	ds_read_b64 v[42:43], v219 offset:24576
	ds_read_b64 v[44:45], v219 offset:28672
	s_waitcnt lgkmcnt(4)
	ds_read_b64 v[46:47], v219 offset:32768
	ds_read_b64 v[48:49], v219 offset:36864
	ds_read_b64 v[50:51], v219 offset:40960
	ds_read_b64 v[52:53], v219 offset:45056
	ds_read_b64 v[54:55], v219 offset:49152
	ds_read_b64 v[56:57], v219 offset:53248
	ds_read_b64 v[58:59], v219 offset:57344
	ds_read_b64 v[60:61], v219 offset:61440
	s_waitcnt lgkmcnt(4)
	ds_read_b64 v[62:63], v220 offset:0
	ds_read_b64 v[64:65], v220 offset:4096
	ds_read_b64 v[66:67], v220 offset:8192
	ds_read_b64 v[68:69], v220 offset:12288
	ds_read_b64 v[70:71], v220 offset:16384
	ds_read_b64 v[72:73], v220 offset:20480
	ds_read_b64 v[74:75], v220 offset:24576
	ds_read_b64 v[76:77], v220 offset:28672
	s_waitcnt lgkmcnt(4)
	ds_read_b64 v[78:79], v220 offset:32768
	ds_read_b64 v[80:81], v220 offset:36864
	ds_read_b64 v[82:83], v220 offset:40960
	ds_read_b64 v[84:85], v220 offset:45056
	ds_read_b64 v[86:87], v220 offset:49152
	ds_read_b64 v[88:89], v220 offset:53248
	ds_read_b64 v[90:91], v220 offset:57344
	ds_read_b64 v[92:93], v220 offset:61440
	s_waitcnt lgkmcnt(4)
	ds_read_b64 v[94:95], v221 offset:0
	ds_read_b64 v[96:97], v221 offset:4096
	ds_read_b64 v[98:99], v221 offset:8192
	ds_read_b64 v[100:101], v221 offset:12288
	ds_write2_b32 v215, v146, v147 offset1:16
	ds_write2_b32 v215, v148, v149 offset0:32 offset1:48
	s_waitcnt lgkmcnt(0)
	s_barrier
	ds_read2st64_b32 v[230:231], v216 offset0:32 offset1:48
	ds_read2st64_b32 v[232:233], v216 offset0:40 offset1:56
	v_cmp_gt_u32_e32 vcc, 18, v213
	s_waitcnt vmcnt(0) lgkmcnt(0)
	v_add_f32_e32 v223, v230, v231
	v_add_f32_e32 v224, v232, v233
	v_add_f32_e32 v223, v223, v254
	v_add_f32_e32 v224, v224, v255
	v_max_f32_e32 v223, 0, v223
	v_max_f32_e32 v224, 0, v224
	v_mov_b32_e32 v226, 0xf149f2ca
	v_cndmask_b32_e32 v224, v226, v224, vcc
	v_max_f32_e32 v225, v223, v224
	s_nop 1
	v_max_f32_dpp v226, v225, v225 quad_perm:[1,0,3,2] row_mask:0xf bank_mask:0xf
	s_nop 1
	v_max_f32_dpp v225, v226, v226 quad_perm:[2,3,0,1] row_mask:0xf bank_mask:0xf
	s_nop 1
	v_max_f32_dpp v226, v225, v225 row_half_mirror row_mask:0xf bank_mask:0xf
	s_nop 1
	v_max_f32_dpp v225, v226, v226 row_mirror row_mask:0xf bank_mask:0xf
	ds_swizzle_b32 v226, v225 offset:swizzle(SWAP,16)
	s_waitcnt lgkmcnt(0)
	v_max_f32_e32 v225, v225, v226
	v_sub_f32_e32 v223, v223, v225
	v_sub_f32_e32 v224, v224, v225
	v_mul_f32_e32 v223, 0x3fb8aa3b, v223
	v_mul_f32_e32 v224, 0x3fb8aa3b, v224
	v_exp_f32_e32 v227, v223
	v_exp_f32_e32 v228, v224
	s_nop 0
	v_add_f32_e32 v229, v227, v228
	s_nop 1
	v_add_f32_dpp v226, v229, v229 quad_perm:[1,0,3,2] row_mask:0xf bank_mask:0xf
	s_nop 1
	v_add_f32_dpp v229, v226, v226 quad_perm:[2,3,0,1] row_mask:0xf bank_mask:0xf
	s_nop 1
	v_add_f32_dpp v226, v229, v229 row_half_mirror row_mask:0xf bank_mask:0xf
	s_nop 1
	v_add_f32_dpp v229, v226, v226 row_mirror row_mask:0xf bank_mask:0xf
	ds_swizzle_b32 v226, v229 offset:swizzle(SWAP,16)
	s_waitcnt lgkmcnt(0)
	v_add_f32_e32 v229, v229, v226
	v_rcp_f32_e32 v234, v229
	s_nop 0
	v_mul_f32_e32 v227, v227, v234
	v_mul_f32_e32 v228, v228, v234
	ds_write_b32 v217, v227
	ds_write_b32 v217, v228 offset:128
	s_waitcnt lgkmcnt(0)
	s_barrier
	ds_read_b128 v[102:105], v218 offset:0
	ds_read_b128 v[106:109], v218 offset:16
	ds_read_b128 v[110:113], v218 offset:32
	ds_read_b128 v[114:117], v218 offset:48
	ds_read_b128 v[118:121], v218 offset:64
	ds_read_b128 v[122:125], v218 offset:80
	ds_read_b128 v[126:129], v218 offset:96
	ds_read_b128 v[130:133], v218 offset:112
	ds_read_b128 v[134:137], v218 offset:128
	ds_read_b128 v[138:141], v218 offset:144
	ds_read_b128 v[142:145], v218 offset:160
	ds_read_b128 v[146:149], v218 offset:176
	ds_read_b128 v[150:153], v218 offset:192
	v_mov_b32_e32 v154, 0
	v_mov_b32_e32 v155, 0
	v_mov_b32_e32 v156, 0
	v_mov_b32_e32 v157, 0
	s_waitcnt vmcnt(0) lgkmcnt(0)
	v_fma_mix_f32 v154, v174, v102, v154 op_sel_hi:[1,0,0]
	v_fma_mix_f32 v155, v174, v102, v155 op_sel:[1,0,0] op_sel_hi:[1,0,0]
	v_fma_mix_f32 v156, v175, v102, v156 op_sel_hi:[1,0,0]
	v_fma_mix_f32 v157, v175, v102, v157 op_sel:[1,0,0] op_sel_hi:[1,0,0]
	v_fma_mix_f32 v154, v176, v103, v154 op_sel_hi:[1,0,0]
	v_fma_mix_f32 v155, v176, v103, v155 op_sel:[1,0,0] op_sel_hi:[1,0,0]
	v_fma_mix_f32 v156, v177, v103, v156 op_sel_hi:[1,0,0]
	v_fma_mix_f32 v157, v177, v103, v157 op_sel:[1,0,0] op_sel_hi:[1,0,0]
	v_fma_mix_f32 v154, v178, v104, v154 op_sel_hi:[1,0,0]
	v_fma_mix_f32 v155, v178, v104, v155 op_sel:[1,0,0] op_sel_hi:[1,0,0]
	v_fma_mix_f32 v156, v179, v104, v156 op_sel_hi:[1,0,0]
	v_fma_mix_f32 v157, v179, v104, v157 op_sel:[1,0,0] op_sel_hi:[1,0,0]
	v_fma_mix_f32 v154, v180, v105, v154 op_sel_hi:[1,0,0]
	v_fma_mix_f32 v155, v180, v105, v155 op_sel:[1,0,0] op_sel_hi:[1,0,0]
	v_fma_mix_f32 v156, v181, v105, v156 op_sel_hi:[1,0,0]
	v_fma_mix_f32 v157, v181, v105, v157 op_sel:[1,0,0] op_sel_hi:[1,0,0]
	v_fma_mix_f32 v154, v182, v106, v154 op_sel_hi:[1,0,0]
	v_fma_mix_f32 v155, v182, v106, v155 op_sel:[1,0,0] op_sel_hi:[1,0,0]
	v_fma_mix_f32 v156, v183, v106, v156 op_sel_hi:[1,0,0]
	v_fma_mix_f32 v157, v183, v106, v157 op_sel:[1,0,0] op_sel_hi:[1,0,0]
	v_fma_mix_f32 v154, v184, v107, v154 op_sel_hi:[1,0,0]
	v_fma_mix_f32 v155, v184, v107, v155 op_sel:[1,0,0] op_sel_hi:[1,0,0]
	v_fma_mix_f32 v156, v185, v107, v156 op_sel_hi:[1,0,0]
	v_fma_mix_f32 v157, v185, v107, v157 op_sel:[1,0,0] op_sel_hi:[1,0,0]
	v_fma_mix_f32 v154, v237, v108, v154 op_sel_hi:[1,0,0]
	v_fma_mix_f32 v155, v237, v108, v155 op_sel:[1,0,0] op_sel_hi:[1,0,0]
	v_fma_mix_f32 v156, v238, v108, v156 op_sel_hi:[1,0,0]
	v_fma_mix_f32 v157, v238, v108, v157 op_sel:[1,0,0] op_sel_hi:[1,0,0]
	v_fma_mix_f32 v154, v239, v109, v154 op_sel_hi:[1,0,0]
	v_fma_mix_f32 v155, v239, v109, v155 op_sel:[1,0,0] op_sel_hi:[1,0,0]
	v_fma_mix_f32 v156, v240, v109, v156 op_sel_hi:[1,0,0]
	v_fma_mix_f32 v157, v240, v109, v157 op_sel:[1,0,0] op_sel_hi:[1,0,0]
	v_fma_mix_f32 v154, v241, v110, v154 op_sel_hi:[1,0,0]
	v_fma_mix_f32 v155, v241, v110, v155 op_sel:[1,0,0] op_sel_hi:[1,0,0]
	v_fma_mix_f32 v156, v242, v110, v156 op_sel_hi:[1,0,0]
	v_fma_mix_f32 v157, v242, v110, v157 op_sel:[1,0,0] op_sel_hi:[1,0,0]
	v_fma_mix_f32 v154, v243, v111, v154 op_sel_hi:[1,0,0]
	v_fma_mix_f32 v155, v243, v111, v155 op_sel:[1,0,0] op_sel_hi:[1,0,0]
	v_fma_mix_f32 v156, v244, v111, v156 op_sel_hi:[1,0,0]
	v_fma_mix_f32 v157, v244, v111, v157 op_sel:[1,0,0] op_sel_hi:[1,0,0]
	v_fma_mix_f32 v154, v245, v112, v154 op_sel_hi:[1,0,0]
	v_fma_mix_f32 v155, v245, v112, v155 op_sel:[1,0,0] op_sel_hi:[1,0,0]
	v_fma_mix_f32 v156, v187, v112, v156 op_sel_hi:[1,0,0]
	v_fma_mix_f32 v157, v187, v112, v157 op_sel:[1,0,0] op_sel_hi:[1,0,0]
	v_fma_mix_f32 v154, v188, v113, v154 op_sel_hi:[1,0,0]
	v_fma_mix_f32 v155, v188, v113, v155 op_sel:[1,0,0] op_sel_hi:[1,0,0]
	v_fma_mix_f32 v156, v202, v113, v156 op_sel_hi:[1,0,0]
	v_fma_mix_f32 v157, v202, v113, v157 op_sel:[1,0,0] op_sel_hi:[1,0,0]
	v_fma_mix_f32 v154, v203, v114, v154 op_sel_hi:[1,0,0]
	v_fma_mix_f32 v155, v203, v114, v155 op_sel:[1,0,0] op_sel_hi:[1,0,0]
	v_fma_mix_f32 v156, v204, v114, v156 op_sel_hi:[1,0,0]
	v_fma_mix_f32 v157, v204, v114, v157 op_sel:[1,0,0] op_sel_hi:[1,0,0]
	v_fma_mix_f32 v154, v205, v115, v154 op_sel_hi:[1,0,0]
	v_fma_mix_f32 v155, v205, v115, v155 op_sel:[1,0,0] op_sel_hi:[1,0,0]
	v_fma_mix_f32 v156, v207, v115, v156 op_sel_hi:[1,0,0]
	v_fma_mix_f32 v157, v207, v115, v157 op_sel:[1,0,0] op_sel_hi:[1,0,0]
	v_fma_mix_f32 v154, v30, v116, v154 op_sel_hi:[1,0,0]
	v_fma_mix_f32 v155, v30, v116, v155 op_sel:[1,0,0] op_sel_hi:[1,0,0]
	v_fma_mix_f32 v156, v31, v116, v156 op_sel_hi:[1,0,0]
	v_fma_mix_f32 v157, v31, v116, v157 op_sel:[1,0,0] op_sel_hi:[1,0,0]
	v_fma_mix_f32 v154, v32, v117, v154 op_sel_hi:[1,0,0]
	v_fma_mix_f32 v155, v32, v117, v155 op_sel:[1,0,0] op_sel_hi:[1,0,0]
	v_fma_mix_f32 v156, v33, v117, v156 op_sel_hi:[1,0,0]
	v_fma_mix_f32 v157, v33, v117, v157 op_sel:[1,0,0] op_sel_hi:[1,0,0]
	v_fma_mix_f32 v154, v34, v118, v154 op_sel_hi:[1,0,0]
	v_fma_mix_f32 v155, v34, v118, v155 op_sel:[1,0,0] op_sel_hi:[1,0,0]
	v_fma_mix_f32 v156, v35, v118, v156 op_sel_hi:[1,0,0]
	v_fma_mix_f32 v157, v35, v118, v157 op_sel:[1,0,0] op_sel_hi:[1,0,0]
	v_fma_mix_f32 v154, v36, v119, v154 op_sel_hi:[1,0,0]
	v_fma_mix_f32 v155, v36, v119, v155 op_sel:[1,0,0] op_sel_hi:[1,0,0]
	v_fma_mix_f32 v156, v37, v119, v156 op_sel_hi:[1,0,0]
	v_fma_mix_f32 v157, v37, v119, v157 op_sel:[1,0,0] op_sel_hi:[1,0,0]
	v_fma_mix_f32 v154, v38, v120, v154 op_sel_hi:[1,0,0]
	v_fma_mix_f32 v155, v38, v120, v155 op_sel:[1,0,0] op_sel_hi:[1,0,0]
	v_fma_mix_f32 v156, v39, v120, v156 op_sel_hi:[1,0,0]
	v_fma_mix_f32 v157, v39, v120, v157 op_sel:[1,0,0] op_sel_hi:[1,0,0]
	v_fma_mix_f32 v154, v40, v121, v154 op_sel_hi:[1,0,0]
	v_fma_mix_f32 v155, v40, v121, v155 op_sel:[1,0,0] op_sel_hi:[1,0,0]
	v_fma_mix_f32 v156, v41, v121, v156 op_sel_hi:[1,0,0]
	v_fma_mix_f32 v157, v41, v121, v157 op_sel:[1,0,0] op_sel_hi:[1,0,0]
	v_fma_mix_f32 v154, v42, v122, v154 op_sel_hi:[1,0,0]
	v_fma_mix_f32 v155, v42, v122, v155 op_sel:[1,0,0] op_sel_hi:[1,0,0]
	v_fma_mix_f32 v156, v43, v122, v156 op_sel_hi:[1,0,0]
	v_fma_mix_f32 v157, v43, v122, v157 op_sel:[1,0,0] op_sel_hi:[1,0,0]
	v_fma_mix_f32 v154, v44, v123, v154 op_sel_hi:[1,0,0]
	v_fma_mix_f32 v155, v44, v123, v155 op_sel:[1,0,0] op_sel_hi:[1,0,0]
	v_fma_mix_f32 v156, v45, v123, v156 op_sel_hi:[1,0,0]
	v_fma_mix_f32 v157, v45, v123, v157 op_sel:[1,0,0] op_sel_hi:[1,0,0]
	v_fma_mix_f32 v154, v46, v124, v154 op_sel_hi:[1,0,0]
	v_fma_mix_f32 v155, v46, v124, v155 op_sel:[1,0,0] op_sel_hi:[1,0,0]
	v_fma_mix_f32 v156, v47, v124, v156 op_sel_hi:[1,0,0]
	v_fma_mix_f32 v157, v47, v124, v157 op_sel:[1,0,0] op_sel_hi:[1,0,0]
	v_fma_mix_f32 v154, v48, v125, v154 op_sel_hi:[1,0,0]
	v_fma_mix_f32 v155, v48, v125, v155 op_sel:[1,0,0] op_sel_hi:[1,0,0]
	v_fma_mix_f32 v156, v49, v125, v156 op_sel_hi:[1,0,0]
	v_fma_mix_f32 v157, v49, v125, v157 op_sel:[1,0,0] op_sel_hi:[1,0,0]
	v_fma_mix_f32 v154, v50, v126, v154 op_sel_hi:[1,0,0]
	v_fma_mix_f32 v155, v50, v126, v155 op_sel:[1,0,0] op_sel_hi:[1,0,0]
	v_fma_mix_f32 v156, v51, v126, v156 op_sel_hi:[1,0,0]
	v_fma_mix_f32 v157, v51, v126, v157 op_sel:[1,0,0] op_sel_hi:[1,0,0]
	v_fma_mix_f32 v154, v52, v127, v154 op_sel_hi:[1,0,0]
	v_fma_mix_f32 v155, v52, v127, v155 op_sel:[1,0,0] op_sel_hi:[1,0,0]
	v_fma_mix_f32 v156, v53, v127, v156 op_sel_hi:[1,0,0]
	v_fma_mix_f32 v157, v53, v127, v157 op_sel:[1,0,0] op_sel_hi:[1,0,0]
	v_fma_mix_f32 v154, v54, v128, v154 op_sel_hi:[1,0,0]
	v_fma_mix_f32 v155, v54, v128, v155 op_sel:[1,0,0] op_sel_hi:[1,0,0]
	v_fma_mix_f32 v156, v55, v128, v156 op_sel_hi:[1,0,0]
	v_fma_mix_f32 v157, v55, v128, v157 op_sel:[1,0,0] op_sel_hi:[1,0,0]
	v_fma_mix_f32 v154, v56, v129, v154 op_sel_hi:[1,0,0]
	v_fma_mix_f32 v155, v56, v129, v155 op_sel:[1,0,0] op_sel_hi:[1,0,0]
	v_fma_mix_f32 v156, v57, v129, v156 op_sel_hi:[1,0,0]
	v_fma_mix_f32 v157, v57, v129, v157 op_sel:[1,0,0] op_sel_hi:[1,0,0]
	v_fma_mix_f32 v154, v58, v130, v154 op_sel_hi:[1,0,0]
	v_fma_mix_f32 v155, v58, v130, v155 op_sel:[1,0,0] op_sel_hi:[1,0,0]
	v_fma_mix_f32 v156, v59, v130, v156 op_sel_hi:[1,0,0]
	v_fma_mix_f32 v157, v59, v130, v157 op_sel:[1,0,0] op_sel_hi:[1,0,0]
	v_fma_mix_f32 v154, v60, v131, v154 op_sel_hi:[1,0,0]
	v_fma_mix_f32 v155, v60, v131, v155 op_sel:[1,0,0] op_sel_hi:[1,0,0]
	v_fma_mix_f32 v156, v61, v131, v156 op_sel_hi:[1,0,0]
	v_fma_mix_f32 v157, v61, v131, v157 op_sel:[1,0,0] op_sel_hi:[1,0,0]
	v_fma_mix_f32 v154, v62, v132, v154 op_sel_hi:[1,0,0]
	v_fma_mix_f32 v155, v62, v132, v155 op_sel:[1,0,0] op_sel_hi:[1,0,0]
	v_fma_mix_f32 v156, v63, v132, v156 op_sel_hi:[1,0,0]
	v_fma_mix_f32 v157, v63, v132, v157 op_sel:[1,0,0] op_sel_hi:[1,0,0]
	v_fma_mix_f32 v154, v64, v133, v154 op_sel_hi:[1,0,0]
	v_fma_mix_f32 v155, v64, v133, v155 op_sel:[1,0,0] op_sel_hi:[1,0,0]
	v_fma_mix_f32 v156, v65, v133, v156 op_sel_hi:[1,0,0]
	v_fma_mix_f32 v157, v65, v133, v157 op_sel:[1,0,0] op_sel_hi:[1,0,0]
	v_fma_mix_f32 v154, v66, v134, v154 op_sel_hi:[1,0,0]
	v_fma_mix_f32 v155, v66, v134, v155 op_sel:[1,0,0] op_sel_hi:[1,0,0]
	v_fma_mix_f32 v156, v67, v134, v156 op_sel_hi:[1,0,0]
	v_fma_mix_f32 v157, v67, v134, v157 op_sel:[1,0,0] op_sel_hi:[1,0,0]
	v_fma_mix_f32 v154, v68, v135, v154 op_sel_hi:[1,0,0]
	v_fma_mix_f32 v155, v68, v135, v155 op_sel:[1,0,0] op_sel_hi:[1,0,0]
	v_fma_mix_f32 v156, v69, v135, v156 op_sel_hi:[1,0,0]
	v_fma_mix_f32 v157, v69, v135, v157 op_sel:[1,0,0] op_sel_hi:[1,0,0]
	v_fma_mix_f32 v154, v70, v136, v154 op_sel_hi:[1,0,0]
	v_fma_mix_f32 v155, v70, v136, v155 op_sel:[1,0,0] op_sel_hi:[1,0,0]
	v_fma_mix_f32 v156, v71, v136, v156 op_sel_hi:[1,0,0]
	v_fma_mix_f32 v157, v71, v136, v157 op_sel:[1,0,0] op_sel_hi:[1,0,0]
	v_fma_mix_f32 v154, v72, v137, v154 op_sel_hi:[1,0,0]
	v_fma_mix_f32 v155, v72, v137, v155 op_sel:[1,0,0] op_sel_hi:[1,0,0]
	v_fma_mix_f32 v156, v73, v137, v156 op_sel_hi:[1,0,0]
	v_fma_mix_f32 v157, v73, v137, v157 op_sel:[1,0,0] op_sel_hi:[1,0,0]
	v_fma_mix_f32 v154, v74, v138, v154 op_sel_hi:[1,0,0]
	v_fma_mix_f32 v155, v74, v138, v155 op_sel:[1,0,0] op_sel_hi:[1,0,0]
	v_fma_mix_f32 v156, v75, v138, v156 op_sel_hi:[1,0,0]
	v_fma_mix_f32 v157, v75, v138, v157 op_sel:[1,0,0] op_sel_hi:[1,0,0]
	v_fma_mix_f32 v154, v76, v139, v154 op_sel_hi:[1,0,0]
	v_fma_mix_f32 v155, v76, v139, v155 op_sel:[1,0,0] op_sel_hi:[1,0,0]
	v_fma_mix_f32 v156, v77, v139, v156 op_sel_hi:[1,0,0]
	v_fma_mix_f32 v157, v77, v139, v157 op_sel:[1,0,0] op_sel_hi:[1,0,0]
	v_fma_mix_f32 v154, v78, v140, v154 op_sel_hi:[1,0,0]
	v_fma_mix_f32 v155, v78, v140, v155 op_sel:[1,0,0] op_sel_hi:[1,0,0]
	v_fma_mix_f32 v156, v79, v140, v156 op_sel_hi:[1,0,0]
	v_fma_mix_f32 v157, v79, v140, v157 op_sel:[1,0,0] op_sel_hi:[1,0,0]
	v_fma_mix_f32 v154, v80, v141, v154 op_sel_hi:[1,0,0]
	v_fma_mix_f32 v155, v80, v141, v155 op_sel:[1,0,0] op_sel_hi:[1,0,0]
	v_fma_mix_f32 v156, v81, v141, v156 op_sel_hi:[1,0,0]
	v_fma_mix_f32 v157, v81, v141, v157 op_sel:[1,0,0] op_sel_hi:[1,0,0]
	v_fma_mix_f32 v154, v82, v142, v154 op_sel_hi:[1,0,0]
	v_fma_mix_f32 v155, v82, v142, v155 op_sel:[1,0,0] op_sel_hi:[1,0,0]
	v_fma_mix_f32 v156, v83, v142, v156 op_sel_hi:[1,0,0]
	v_fma_mix_f32 v157, v83, v142, v157 op_sel:[1,0,0] op_sel_hi:[1,0,0]
	v_fma_mix_f32 v154, v84, v143, v154 op_sel_hi:[1,0,0]
	v_fma_mix_f32 v155, v84, v143, v155 op_sel:[1,0,0] op_sel_hi:[1,0,0]
	v_fma_mix_f32 v156, v85, v143, v156 op_sel_hi:[1,0,0]
	v_fma_mix_f32 v157, v85, v143, v157 op_sel:[1,0,0] op_sel_hi:[1,0,0]
	v_fma_mix_f32 v154, v86, v144, v154 op_sel_hi:[1,0,0]
	v_fma_mix_f32 v155, v86, v144, v155 op_sel:[1,0,0] op_sel_hi:[1,0,0]
	v_fma_mix_f32 v156, v87, v144, v156 op_sel_hi:[1,0,0]
	v_fma_mix_f32 v157, v87, v144, v157 op_sel:[1,0,0] op_sel_hi:[1,0,0]
	v_fma_mix_f32 v154, v88, v145, v154 op_sel_hi:[1,0,0]
	v_fma_mix_f32 v155, v88, v145, v155 op_sel:[1,0,0] op_sel_hi:[1,0,0]
	v_fma_mix_f32 v156, v89, v145, v156 op_sel_hi:[1,0,0]
	v_fma_mix_f32 v157, v89, v145, v157 op_sel:[1,0,0] op_sel_hi:[1,0,0]
	v_fma_mix_f32 v154, v90, v146, v154 op_sel_hi:[1,0,0]
	v_fma_mix_f32 v155, v90, v146, v155 op_sel:[1,0,0] op_sel_hi:[1,0,0]
	v_fma_mix_f32 v156, v91, v146, v156 op_sel_hi:[1,0,0]
	v_fma_mix_f32 v157, v91, v146, v157 op_sel:[1,0,0] op_sel_hi:[1,0,0]
	v_fma_mix_f32 v154, v92, v147, v154 op_sel_hi:[1,0,0]
	v_fma_mix_f32 v155, v92, v147, v155 op_sel:[1,0,0] op_sel_hi:[1,0,0]
	v_fma_mix_f32 v156, v93, v147, v156 op_sel_hi:[1,0,0]
	v_fma_mix_f32 v157, v93, v147, v157 op_sel:[1,0,0] op_sel_hi:[1,0,0]
	v_fma_mix_f32 v154, v94, v148, v154 op_sel_hi:[1,0,0]
	v_fma_mix_f32 v155, v94, v148, v155 op_sel:[1,0,0] op_sel_hi:[1,0,0]
	v_fma_mix_f32 v156, v95, v148, v156 op_sel_hi:[1,0,0]
	v_fma_mix_f32 v157, v95, v148, v157 op_sel:[1,0,0] op_sel_hi:[1,0,0]
	v_fma_mix_f32 v154, v96, v149, v154 op_sel_hi:[1,0,0]
	v_fma_mix_f32 v155, v96, v149, v155 op_sel:[1,0,0] op_sel_hi:[1,0,0]
	v_fma_mix_f32 v156, v97, v149, v156 op_sel_hi:[1,0,0]
	v_fma_mix_f32 v157, v97, v149, v157 op_sel:[1,0,0] op_sel_hi:[1,0,0]
	v_fma_mix_f32 v154, v98, v150, v154 op_sel_hi:[1,0,0]
	v_fma_mix_f32 v155, v98, v150, v155 op_sel:[1,0,0] op_sel_hi:[1,0,0]
	v_fma_mix_f32 v156, v99, v150, v156 op_sel_hi:[1,0,0]
	v_fma_mix_f32 v157, v99, v150, v157 op_sel:[1,0,0] op_sel_hi:[1,0,0]
	v_fma_mix_f32 v154, v100, v151, v154 op_sel_hi:[1,0,0]
	v_fma_mix_f32 v155, v100, v151, v155 op_sel:[1,0,0] op_sel_hi:[1,0,0]
	v_fma_mix_f32 v156, v101, v151, v156 op_sel_hi:[1,0,0]
	v_fma_mix_f32 v157, v101, v151, v157 op_sel:[1,0,0] op_sel_hi:[1,0,0]
	global_store_dwordx4 v222, v[154:157], s[8:9]
	s_endpgm
